# speedup vs baseline: 1.0407x; 1.0037x over previous
.LBB1_3:
	s_waitcnt lgkmcnt(0)
	v_mfma_f32_32x32x16_f16 a[0:15], v[18:21], v[74:77], a[0:15]
	s_add_i32 s31, s30, 1
	s_cmp_lg_u32 s30, 2
	s_cselect_b32 s91, s31, 0
	s_mul_i32 s30, s30, 0x9000
	s_mul_i32 s92, s91, 0x9000
	v_add_u32_e32 v147, s30, v208
	v_add_u32_e32 v2, s30, v209
	v_add_u32_e32 v3, s30, v210
	v_add_u32_e32 v146, s92, v141
	s_add_u32 s30, s35, s20
	s_addc_u32 s31, s84, s21
	s_add_i32 s96, s92, 0x9000
	s_cmp_lg_u32 s91, 2
	s_cselect_b32 s96, s96, 0
	s_add_i32 s96, s96, s93
	s_mov_b32 m0, s96
	s_nop 0
	global_load_lds_dwordx4 v164, s[94:95]
	s_add_u32 m0, s96, 0x1000
	s_nop 0
	global_load_lds_dwordx4 v165, s[94:95]
	s_add_u32 m0, s96, 0x2000
	s_nop 0
	global_load_lds_dwordx4 v166, s[94:95]
	s_add_u32 m0, s96, 0x3000
	s_nop 0
	global_load_lds_dwordx4 v167, s[94:95]
	s_add_u32 m0, s96, 0x4000
	s_nop 0
	global_load_lds_dwordx4 v168, s[94:95]
	s_add_u32 m0, s96, 0x5000
	s_nop 0
	global_load_lds_dwordx4 v169, s[94:95]
	s_add_u32 m0, s96, 0x6000
	s_nop 0
	global_load_lds_dwordx4 v170, s[94:95]
	s_add_u32 m0, s96, 0x7000
	s_nop 0
	global_load_lds_dwordx4 v171, s[94:95]
	s_load_dwordx16 s[68:83], s[30:31], 0x80
	s_load_dwordx16 s[52:67], s[30:31], 0x8080
	ds_read_b128 v[90:93], v145
	ds_read_b128 v[82:85], v145 offset:2048
	v_mfma_f32_32x32x16_f16 a[240:255], v[38:41], v[74:77], a[240:255]
	ds_read_b128 v[50:53], v147
	v_pk_mul_f16 v148, v46, v136
	v_pk_mul_f16 v149, v42, v137
	v_pk_mul_f16 v150, v47, v136
	v_pk_mul_f16 v151, v43, v137
	v_mfma_f32_32x32x16_f16 a[16:31], v[18:21], v[126:129], a[16:31]
	ds_read_b128 v[54:57], v147 offset:4096
	v_pk_mul_f16 v152, v48, v136
	v_pk_mul_f16 v153, v44, v137
	v_pk_mul_f16 v154, v49, v136
	v_pk_mul_f16 v155, v45, v137
	v_mfma_f32_32x32x16_f16 a[224:239], v[38:41], v[126:129], a[224:239]
	ds_read_b128 v[58:61], v147 offset:8192
	v_pk_mul_f16 v156, v46, v140
	v_pk_mul_f16 v157, v42, v139
	v_pk_mul_f16 v158, v47, v140
	v_pk_mul_f16 v159, v43, v139
	v_mfma_f32_32x32x16_f16 a[32:47], v[18:21], v[122:125], a[32:47]
	ds_read_b128 v[62:65], v147 offset:12288
	v_pk_mul_f16 v160, v48, v140
	v_pk_mul_f16 v161, v44, v139
	v_pk_mul_f16 v162, v49, v140
	v_pk_mul_f16 v163, v45, v139
	v_mfma_f32_32x32x16_f16 a[208:223], v[38:41], v[122:125], a[208:223]
	ds_read_b128 v[66:69], v147 offset:16384
	v_pk_max_f16 v148, v148, v149
	v_pk_max_f16 v150, v150, v151
	v_pk_max_f16 v152, v152, v153
	v_pk_max_f16 v154, v154, v155
	v_mfma_f32_32x32x16_f16 a[48:63], v[18:21], v[118:121], a[48:63]
	ds_read_b128 v[70:73], v147 offset:20480
	v_pk_max_f16 v156, v156, v157
	v_pk_max_f16 v158, v158, v159
	v_pk_max_f16 v160, v160, v161
	v_pk_max_f16 v162, v162, v163
	v_mfma_f32_32x32x16_f16 a[192:207], v[38:41], v[118:121], a[192:207]
	ds_read_b128 v[78:81], v147 offset:24576
	v_cndmask_b32_e64 v114, v1, v148, s[36:37]
	s_mov_b64 vcc, s[38:39]
	v_cndmask_b32_sdwa v114, v1, v148, vcc dst_sel:WORD_1 dst_unused:UNUSED_PRESERVE src0_sel:WORD_1 src1_sel:WORD_1
	v_cndmask_b32_e64 v115, v1, v150, s[40:41]
	s_mov_b64 vcc, s[42:43]
	v_cndmask_b32_sdwa v115, v1, v150, vcc dst_sel:WORD_1 dst_unused:UNUSED_PRESERVE src0_sel:WORD_1 src1_sel:WORD_1
	v_mfma_f32_32x32x16_f16 a[64:79], v[18:21], v[106:109], a[64:79]
	ds_read_b128 v[102:105], v147 offset:28672
	v_cndmask_b32_e64 v116, v1, v152, s[44:45]
	s_mov_b64 vcc, s[46:47]
	v_cndmask_b32_sdwa v116, v1, v152, vcc dst_sel:WORD_1 dst_unused:UNUSED_PRESERVE src0_sel:WORD_1 src1_sel:WORD_1
	v_cndmask_b32_e64 v117, v1, v154, s[48:49]
	s_mov_b64 vcc, s[50:51]
	v_cndmask_b32_sdwa v117, v1, v154, vcc dst_sel:WORD_1 dst_unused:UNUSED_PRESERVE src0_sel:WORD_1 src1_sel:WORD_1
	v_mfma_f32_32x32x16_f16 a[176:191], v[38:41], v[106:109], a[176:191]
	v_cndmask_b32_e64 v110, v138, v156, s[4:5]
	s_mov_b64 vcc, s[6:7]
	v_cndmask_b32_sdwa v110, v138, v156, vcc dst_sel:WORD_1 dst_unused:UNUSED_PRESERVE src0_sel:WORD_1 src1_sel:WORD_1
	v_cndmask_b32_e64 v111, v138, v158, s[8:9]
	s_mov_b64 vcc, s[10:11]
	v_cndmask_b32_sdwa v111, v138, v158, vcc dst_sel:WORD_1 dst_unused:UNUSED_PRESERVE src0_sel:WORD_1 src1_sel:WORD_1
	v_mfma_f32_32x32x16_f16 a[112:127], v[18:21], v[98:101], a[112:127]
	v_cndmask_b32_e64 v112, v138, v160, s[12:13]
	s_mov_b64 vcc, s[14:15]
	v_cndmask_b32_sdwa v112, v138, v160, vcc dst_sel:WORD_1 dst_unused:UNUSED_PRESERVE src0_sel:WORD_1 src1_sel:WORD_1
	v_cndmask_b32_e64 v113, v138, v162, s[16:17]
	s_mov_b64 vcc, s[18:19]
	v_cndmask_b32_sdwa v113, v138, v162, vcc dst_sel:WORD_1 dst_unused:UNUSED_PRESERVE src0_sel:WORD_1 src1_sel:WORD_1
	v_mfma_f32_32x32x16_f16 a[160:175], v[38:41], v[98:101], a[160:175]
	v_pk_add_f16 v148, v115, v114
	v_pk_add_f16 v149, v116, v117
	v_mfma_f32_32x32x16_f16 a[128:143], v[18:21], v[94:97], a[128:143]
	v_pk_add_f16 v150, v111, v110
	v_pk_add_f16 v151, v112, v113
	v_mfma_f32_32x32x16_f16 a[144:159], v[38:41], v[94:97], a[144:159]
	v_pk_add_f16 v148, v148, v149
	v_pk_add_f16 v150, v150, v151
	v_mfma_f32_32x32x16_f16 a[80:95], v[18:21], v[86:89], a[80:95]
	v_dot2c_f32_f16_e32 v134, 0x3c003c00, v148
	v_dot2c_f32_f16_e32 v135, 0x3c003c00, v150
	v_mfma_f32_32x32x16_f16 a[96:111], v[38:41], v[86:89], a[96:111]
	s_waitcnt lgkmcnt(0)
	v_mfma_f32_32x32x16_f16 a[0:15], v[114:117], v[50:53], a[0:15]
	s_load_dwordx16 s[36:51], s[30:31], 0xc0
	s_load_dwordx16 s[4:19], s[30:31], 0x80c0
	ds_read_b128 v[46:49], v145 offset:32
	ds_read_b128 v[42:45], v145 offset:2080
	v_mfma_f32_32x32x16_f16 a[240:255], v[110:113], v[50:53], a[240:255]
	ds_read_b128 v[74:77], v2
	v_pk_mul_f16 v148, v90, v136
	v_pk_mul_f16 v149, v82, v137
	v_pk_mul_f16 v150, v91, v136
	v_pk_mul_f16 v151, v83, v137
	v_mfma_f32_32x32x16_f16 a[16:31], v[114:117], v[54:57], a[16:31]
	ds_read_b128 v[126:129], v2 offset:4096
	v_pk_mul_f16 v152, v92, v136
	v_pk_mul_f16 v153, v84, v137
	v_pk_mul_f16 v154, v93, v136
	v_pk_mul_f16 v155, v85, v137
	v_mfma_f32_32x32x16_f16 a[224:239], v[110:113], v[54:57], a[224:239]
	ds_read_b128 v[122:125], v2 offset:8192
	v_pk_mul_f16 v156, v90, v140
	v_pk_mul_f16 v157, v82, v139
	v_pk_mul_f16 v158, v91, v140
	v_pk_mul_f16 v159, v83, v139
	v_mfma_f32_32x32x16_f16 a[32:47], v[114:117], v[58:61], a[32:47]
	ds_read_b128 v[118:121], v2 offset:12288
	v_pk_mul_f16 v160, v92, v140
	v_pk_mul_f16 v161, v84, v139
	v_pk_mul_f16 v162, v93, v140
	v_pk_mul_f16 v163, v85, v139
	v_mfma_f32_32x32x16_f16 a[208:223], v[110:113], v[58:61], a[208:223]
	ds_read_b128 v[106:109], v2 offset:16384
	v_pk_max_f16 v148, v148, v149
	v_pk_max_f16 v150, v150, v151
	v_pk_max_f16 v152, v152, v153
	v_pk_max_f16 v154, v154, v155
	v_mfma_f32_32x32x16_f16 a[48:63], v[114:117], v[62:65], a[48:63]
	ds_read_b128 v[98:101], v2 offset:20480
	v_pk_max_f16 v156, v156, v157
	v_pk_max_f16 v158, v158, v159
	v_pk_max_f16 v160, v160, v161
	v_pk_max_f16 v162, v162, v163
	v_mfma_f32_32x32x16_f16 a[192:207], v[110:113], v[62:65], a[192:207]
	ds_read_b128 v[94:97], v2 offset:24576
	v_cndmask_b32_e64 v18, v1, v148, s[68:69]
	s_mov_b64 vcc, s[70:71]
	v_cndmask_b32_sdwa v18, v1, v148, vcc dst_sel:WORD_1 dst_unused:UNUSED_PRESERVE src0_sel:WORD_1 src1_sel:WORD_1
	v_cndmask_b32_e64 v19, v1, v150, s[72:73]
	s_mov_b64 vcc, s[74:75]
	v_cndmask_b32_sdwa v19, v1, v150, vcc dst_sel:WORD_1 dst_unused:UNUSED_PRESERVE src0_sel:WORD_1 src1_sel:WORD_1
	v_mfma_f32_32x32x16_f16 a[64:79], v[114:117], v[66:69], a[64:79]
	ds_read_b128 v[86:89], v2 offset:28672
	v_cndmask_b32_e64 v20, v1, v152, s[76:77]
	s_mov_b64 vcc, s[78:79]
	v_cndmask_b32_sdwa v20, v1, v152, vcc dst_sel:WORD_1 dst_unused:UNUSED_PRESERVE src0_sel:WORD_1 src1_sel:WORD_1
	v_cndmask_b32_e64 v21, v1, v154, s[80:81]
	s_mov_b64 vcc, s[82:83]
	v_cndmask_b32_sdwa v21, v1, v154, vcc dst_sel:WORD_1 dst_unused:UNUSED_PRESERVE src0_sel:WORD_1 src1_sel:WORD_1
	v_mfma_f32_32x32x16_f16 a[176:191], v[110:113], v[66:69], a[176:191]
	v_cndmask_b32_e64 v38, v138, v156, s[52:53]
	s_mov_b64 vcc, s[54:55]
	v_cndmask_b32_sdwa v38, v138, v156, vcc dst_sel:WORD_1 dst_unused:UNUSED_PRESERVE src0_sel:WORD_1 src1_sel:WORD_1
	v_cndmask_b32_e64 v39, v138, v158, s[56:57]
	s_mov_b64 vcc, s[58:59]
	v_cndmask_b32_sdwa v39, v138, v158, vcc dst_sel:WORD_1 dst_unused:UNUSED_PRESERVE src0_sel:WORD_1 src1_sel:WORD_1
	v_mfma_f32_32x32x16_f16 a[112:127], v[114:117], v[70:73], a[112:127]
	v_cndmask_b32_e64 v40, v138, v160, s[60:61]
	s_mov_b64 vcc, s[62:63]
	v_cndmask_b32_sdwa v40, v138, v160, vcc dst_sel:WORD_1 dst_unused:UNUSED_PRESERVE src0_sel:WORD_1 src1_sel:WORD_1
	v_cndmask_b32_e64 v41, v138, v162, s[64:65]
	s_mov_b64 vcc, s[66:67]
	v_cndmask_b32_sdwa v41, v138, v162, vcc dst_sel:WORD_1 dst_unused:UNUSED_PRESERVE src0_sel:WORD_1 src1_sel:WORD_1
	v_mfma_f32_32x32x16_f16 a[160:175], v[110:113], v[70:73], a[160:175]
	v_pk_add_f16 v148, v19, v18
	v_pk_add_f16 v149, v20, v21
	v_mfma_f32_32x32x16_f16 a[128:143], v[114:117], v[78:81], a[128:143]
	v_pk_add_f16 v150, v39, v38
	v_pk_add_f16 v151, v40, v41
	v_mfma_f32_32x32x16_f16 a[144:159], v[110:113], v[78:81], a[144:159]
	v_pk_add_f16 v148, v148, v149
	v_pk_add_f16 v150, v150, v151
	v_mfma_f32_32x32x16_f16 a[80:95], v[114:117], v[102:105], a[80:95]
	v_dot2c_f32_f16_e32 v134, 0x3c003c00, v148
	v_dot2c_f32_f16_e32 v135, 0x3c003c00, v150
	v_mfma_f32_32x32x16_f16 a[96:111], v[110:113], v[102:105], a[96:111]
	s_waitcnt lgkmcnt(0)
	v_mfma_f32_32x32x16_f16 a[0:15], v[18:21], v[74:77], a[0:15]
	s_load_dwordx16 s[68:83], s[30:31], 0x100
	s_load_dwordx16 s[52:67], s[30:31], 0x8100
	ds_read_b128 v[90:93], v145 offset:64
	ds_read_b128 v[82:85], v145 offset:2112
	v_mfma_f32_32x32x16_f16 a[240:255], v[38:41], v[74:77], a[240:255]
	ds_read_b128 v[50:53], v3
	v_pk_mul_f16 v148, v46, v136
	v_pk_mul_f16 v149, v42, v137
	v_pk_mul_f16 v150, v47, v136
	v_pk_mul_f16 v151, v43, v137
	v_mfma_f32_32x32x16_f16 a[16:31], v[18:21], v[126:129], a[16:31]
	ds_read_b128 v[54:57], v3 offset:4096
	v_pk_mul_f16 v152, v48, v136
	v_pk_mul_f16 v153, v44, v137
	v_pk_mul_f16 v154, v49, v136
	v_pk_mul_f16 v155, v45, v137
	v_mfma_f32_32x32x16_f16 a[224:239], v[38:41], v[126:129], a[224:239]
	ds_read_b128 v[58:61], v3 offset:8192
	v_pk_mul_f16 v156, v46, v140
	v_pk_mul_f16 v157, v42, v139
	v_pk_mul_f16 v158, v47, v140
	v_pk_mul_f16 v159, v43, v139
	v_mfma_f32_32x32x16_f16 a[32:47], v[18:21], v[122:125], a[32:47]
	ds_read_b128 v[62:65], v3 offset:12288
	v_pk_mul_f16 v160, v48, v140
	v_pk_mul_f16 v161, v44, v139
	v_pk_mul_f16 v162, v49, v140
	v_pk_mul_f16 v163, v45, v139
	v_mfma_f32_32x32x16_f16 a[208:223], v[38:41], v[122:125], a[208:223]
	ds_read_b128 v[66:69], v3 offset:16384
	v_pk_max_f16 v148, v148, v149
	v_pk_max_f16 v150, v150, v151
	v_pk_max_f16 v152, v152, v153
	v_pk_max_f16 v154, v154, v155
	v_mfma_f32_32x32x16_f16 a[48:63], v[18:21], v[118:121], a[48:63]
	ds_read_b128 v[70:73], v3 offset:20480
	v_pk_max_f16 v156, v156, v157
	v_pk_max_f16 v158, v158, v159
	v_pk_max_f16 v160, v160, v161
	v_pk_max_f16 v162, v162, v163
	v_mfma_f32_32x32x16_f16 a[192:207], v[38:41], v[118:121], a[192:207]
	ds_read_b128 v[78:81], v3 offset:24576
	v_cndmask_b32_e64 v114, v1, v148, s[36:37]
	s_mov_b64 vcc, s[38:39]
	v_cndmask_b32_sdwa v114, v1, v148, vcc dst_sel:WORD_1 dst_unused:UNUSED_PRESERVE src0_sel:WORD_1 src1_sel:WORD_1
	v_cndmask_b32_e64 v115, v1, v150, s[40:41]
	s_mov_b64 vcc, s[42:43]
	v_cndmask_b32_sdwa v115, v1, v150, vcc dst_sel:WORD_1 dst_unused:UNUSED_PRESERVE src0_sel:WORD_1 src1_sel:WORD_1
	v_mfma_f32_32x32x16_f16 a[64:79], v[18:21], v[106:109], a[64:79]
	ds_read_b128 v[102:105], v3 offset:28672
	v_cndmask_b32_e64 v116, v1, v152, s[44:45]
	s_mov_b64 vcc, s[46:47]
	v_cndmask_b32_sdwa v116, v1, v152, vcc dst_sel:WORD_1 dst_unused:UNUSED_PRESERVE src0_sel:WORD_1 src1_sel:WORD_1
	v_cndmask_b32_e64 v117, v1, v154, s[48:49]
	s_mov_b64 vcc, s[50:51]
	v_cndmask_b32_sdwa v117, v1, v154, vcc dst_sel:WORD_1 dst_unused:UNUSED_PRESERVE src0_sel:WORD_1 src1_sel:WORD_1
	v_mfma_f32_32x32x16_f16 a[176:191], v[38:41], v[106:109], a[176:191]
	v_cndmask_b32_e64 v110, v138, v156, s[4:5]
	s_mov_b64 vcc, s[6:7]
	v_cndmask_b32_sdwa v110, v138, v156, vcc dst_sel:WORD_1 dst_unused:UNUSED_PRESERVE src0_sel:WORD_1 src1_sel:WORD_1
	v_cndmask_b32_e64 v111, v138, v158, s[8:9]
	s_mov_b64 vcc, s[10:11]
	v_cndmask_b32_sdwa v111, v138, v158, vcc dst_sel:WORD_1 dst_unused:UNUSED_PRESERVE src0_sel:WORD_1 src1_sel:WORD_1
	v_mfma_f32_32x32x16_f16 a[112:127], v[18:21], v[98:101], a[112:127]
	v_cndmask_b32_e64 v112, v138, v160, s[12:13]
	s_mov_b64 vcc, s[14:15]
	v_cndmask_b32_sdwa v112, v138, v160, vcc dst_sel:WORD_1 dst_unused:UNUSED_PRESERVE src0_sel:WORD_1 src1_sel:WORD_1
	v_cndmask_b32_e64 v113, v138, v162, s[16:17]
	s_mov_b64 vcc, s[18:19]
	v_cndmask_b32_sdwa v113, v138, v162, vcc dst_sel:WORD_1 dst_unused:UNUSED_PRESERVE src0_sel:WORD_1 src1_sel:WORD_1
	v_mfma_f32_32x32x16_f16 a[160:175], v[38:41], v[98:101], a[160:175]
	v_pk_add_f16 v148, v115, v114
	v_pk_add_f16 v149, v116, v117
	v_mfma_f32_32x32x16_f16 a[128:143], v[18:21], v[94:97], a[128:143]
	v_pk_add_f16 v150, v111, v110
	v_pk_add_f16 v151, v112, v113
	v_mfma_f32_32x32x16_f16 a[144:159], v[38:41], v[94:97], a[144:159]
	v_pk_add_f16 v148, v148, v149
	v_pk_add_f16 v150, v150, v151
	v_mfma_f32_32x32x16_f16 a[80:95], v[18:21], v[86:89], a[80:95]
	v_dot2c_f32_f16_e32 v134, 0x3c003c00, v148
	v_dot2c_f32_f16_e32 v135, 0x3c003c00, v150
	v_mfma_f32_32x32x16_f16 a[96:111], v[38:41], v[86:89], a[96:111]
	s_waitcnt lgkmcnt(0)
	v_mfma_f32_32x32x16_f16 a[0:15], v[114:117], v[50:53], a[0:15]
	s_load_dwordx16 s[36:51], s[30:31], 0x140
	s_load_dwordx16 s[4:19], s[30:31], 0x8140
	ds_read_b128 v[46:49], v145 offset:96
	ds_read_b128 v[42:45], v145 offset:2144
	v_mfma_f32_32x32x16_f16 a[240:255], v[110:113], v[50:53], a[240:255]
	ds_read_b128 v[74:77], v146
	v_pk_mul_f16 v148, v90, v136
	v_pk_mul_f16 v149, v82, v137
	v_pk_mul_f16 v150, v91, v136
	v_pk_mul_f16 v151, v83, v137
	v_mfma_f32_32x32x16_f16 a[16:31], v[114:117], v[54:57], a[16:31]
	ds_read_b128 v[126:129], v146 offset:4096
	v_pk_mul_f16 v152, v92, v136
	v_pk_mul_f16 v153, v84, v137
	v_pk_mul_f16 v154, v93, v136
	v_pk_mul_f16 v155, v85, v137
	v_mfma_f32_32x32x16_f16 a[224:239], v[110:113], v[54:57], a[224:239]
	ds_read_b128 v[122:125], v146 offset:8192
	v_pk_mul_f16 v156, v90, v140
	v_pk_mul_f16 v157, v82, v139
	v_pk_mul_f16 v158, v91, v140
	v_pk_mul_f16 v159, v83, v139
	v_mfma_f32_32x32x16_f16 a[32:47], v[114:117], v[58:61], a[32:47]
	ds_read_b128 v[118:121], v146 offset:12288
	v_pk_mul_f16 v160, v92, v140
	v_pk_mul_f16 v161, v84, v139
	v_pk_mul_f16 v162, v93, v140
	v_pk_mul_f16 v163, v85, v139
	v_mfma_f32_32x32x16_f16 a[208:223], v[110:113], v[58:61], a[208:223]
	ds_read_b128 v[106:109], v146 offset:16384
	v_pk_max_f16 v148, v148, v149
	v_pk_max_f16 v150, v150, v151
	v_pk_max_f16 v152, v152, v153
	v_pk_max_f16 v154, v154, v155
	v_mfma_f32_32x32x16_f16 a[48:63], v[114:117], v[62:65], a[48:63]
	ds_read_b128 v[98:101], v146 offset:20480
	v_pk_max_f16 v156, v156, v157
	v_pk_max_f16 v158, v158, v159
	v_pk_max_f16 v160, v160, v161
	v_pk_max_f16 v162, v162, v163
	v_mfma_f32_32x32x16_f16 a[192:207], v[110:113], v[62:65], a[192:207]
	ds_read_b128 v[94:97], v146 offset:24576
	v_cndmask_b32_e64 v18, v1, v148, s[68:69]
	s_mov_b64 vcc, s[70:71]
	v_cndmask_b32_sdwa v18, v1, v148, vcc dst_sel:WORD_1 dst_unused:UNUSED_PRESERVE src0_sel:WORD_1 src1_sel:WORD_1
	v_cndmask_b32_e64 v19, v1, v150, s[72:73]
	s_mov_b64 vcc, s[74:75]
	v_cndmask_b32_sdwa v19, v1, v150, vcc dst_sel:WORD_1 dst_unused:UNUSED_PRESERVE src0_sel:WORD_1 src1_sel:WORD_1
	v_mfma_f32_32x32x16_f16 a[64:79], v[114:117], v[66:69], a[64:79]
	ds_read_b128 v[86:89], v146 offset:28672
	v_cndmask_b32_e64 v20, v1, v152, s[76:77]
	s_mov_b64 vcc, s[78:79]
	v_cndmask_b32_sdwa v20, v1, v152, vcc dst_sel:WORD_1 dst_unused:UNUSED_PRESERVE src0_sel:WORD_1 src1_sel:WORD_1
	v_cndmask_b32_e64 v21, v1, v154, s[80:81]
	s_mov_b64 vcc, s[82:83]
	v_cndmask_b32_sdwa v21, v1, v154, vcc dst_sel:WORD_1 dst_unused:UNUSED_PRESERVE src0_sel:WORD_1 src1_sel:WORD_1
	v_mfma_f32_32x32x16_f16 a[176:191], v[110:113], v[66:69], a[176:191]
	v_cndmask_b32_e64 v38, v138, v156, s[52:53]
	s_mov_b64 vcc, s[54:55]
	v_cndmask_b32_sdwa v38, v138, v156, vcc dst_sel:WORD_1 dst_unused:UNUSED_PRESERVE src0_sel:WORD_1 src1_sel:WORD_1
	v_cndmask_b32_e64 v39, v138, v158, s[56:57]
	s_mov_b64 vcc, s[58:59]
	v_cndmask_b32_sdwa v39, v138, v158, vcc dst_sel:WORD_1 dst_unused:UNUSED_PRESERVE src0_sel:WORD_1 src1_sel:WORD_1
	v_mfma_f32_32x32x16_f16 a[112:127], v[114:117], v[70:73], a[112:127]
	v_cndmask_b32_e64 v40, v138, v160, s[60:61]
	s_mov_b64 vcc, s[62:63]
	v_cndmask_b32_sdwa v40, v138, v160, vcc dst_sel:WORD_1 dst_unused:UNUSED_PRESERVE src0_sel:WORD_1 src1_sel:WORD_1
	v_cndmask_b32_e64 v41, v138, v162, s[64:65]
	s_mov_b64 vcc, s[66:67]
	v_cndmask_b32_sdwa v41, v138, v162, vcc dst_sel:WORD_1 dst_unused:UNUSED_PRESERVE src0_sel:WORD_1 src1_sel:WORD_1
	v_mfma_f32_32x32x16_f16 a[160:175], v[110:113], v[70:73], a[160:175]
	v_pk_add_f16 v148, v19, v18
	v_pk_add_f16 v149, v20, v21
	v_mfma_f32_32x32x16_f16 a[128:143], v[114:117], v[78:81], a[128:143]
	v_pk_add_f16 v150, v39, v38
	v_pk_add_f16 v151, v40, v41
	v_mfma_f32_32x32x16_f16 a[144:159], v[110:113], v[78:81], a[144:159]
	v_pk_add_f16 v148, v148, v149
	v_pk_add_f16 v150, v150, v151
	v_mfma_f32_32x32x16_f16 a[80:95], v[114:117], v[102:105], a[80:95]
	v_dot2c_f32_f16_e32 v134, 0x3c003c00, v148
	v_dot2c_f32_f16_e32 v135, 0x3c003c00, v150
	v_mfma_f32_32x32x16_f16 a[96:111], v[110:113], v[102:105], a[96:111]
	s_add_i32 s92, s92, 0x9000
	s_cmp_lg_u32 s91, 2
	s_cselect_b32 s30, s92, 0
	s_add_u32 s20, s20, 0x100
	s_addc_u32 s21, s21, 0
	s_add_u32 s94, s94, 0x8000
	s_addc_u32 s95, s95, 0
	v_add_u32_e32 v145, 0x80, v145
	s_cmpk_eq_i32 s20, 0xf00
	s_mov_b32 s30, s91
	s_waitcnt vmcnt(0)
	s_waitcnt lgkmcnt(0)
	s_barrier
	s_cbranch_scc0 .LBB1_3
	s_waitcnt lgkmcnt(0)
	v_mfma_f32_32x32x16_f16 a[0:15], v[18:21], v[74:77], a[0:15]
	s_load_dwordx16 s[68:83], s[0:1], 0xf80
	s_load_dwordx16 s[52:67], s[0:1], 0x8f80
	ds_read_b128 v[90:93], v142 offset:1984
	ds_read_b128 v[82:85], v142 offset:4032
	v_mfma_f32_32x32x16_f16 a[240:255], v[38:41], v[74:77], a[240:255]
	ds_read_b128 v[50:53], v208
	v_pk_mul_f16 v148, v46, v136
	v_pk_mul_f16 v149, v42, v137
	v_pk_mul_f16 v150, v47, v136
	v_pk_mul_f16 v151, v43, v137
	v_mfma_f32_32x32x16_f16 a[16:31], v[18:21], v[126:129], a[16:31]
	ds_read_b128 v[54:57], v208 offset:4096
	v_pk_mul_f16 v152, v48, v136
	v_pk_mul_f16 v153, v44, v137
	v_pk_mul_f16 v154, v49, v136
	v_pk_mul_f16 v155, v45, v137
	v_mfma_f32_32x32x16_f16 a[224:239], v[38:41], v[126:129], a[224:239]
	ds_read_b128 v[58:61], v208 offset:8192
	v_pk_mul_f16 v156, v46, v140
	v_pk_mul_f16 v157, v42, v139
	v_pk_mul_f16 v158, v47, v140
	v_pk_mul_f16 v159, v43, v139
	v_mfma_f32_32x32x16_f16 a[32:47], v[18:21], v[122:125], a[32:47]
	ds_read_b128 v[62:65], v208 offset:12288
	v_pk_mul_f16 v160, v48, v140
	v_pk_mul_f16 v161, v44, v139
	v_pk_mul_f16 v162, v49, v140
	v_pk_mul_f16 v163, v45, v139
	v_mfma_f32_32x32x16_f16 a[208:223], v[38:41], v[122:125], a[208:223]
	ds_read_b128 v[66:69], v208 offset:16384
	v_pk_max_f16 v148, v148, v149
	v_pk_max_f16 v150, v150, v151
	v_pk_max_f16 v152, v152, v153
	v_pk_max_f16 v154, v154, v155
	v_mfma_f32_32x32x16_f16 a[48:63], v[18:21], v[118:121], a[48:63]
	ds_read_b128 v[70:73], v208 offset:20480
	v_pk_max_f16 v156, v156, v157
	v_pk_max_f16 v158, v158, v159
	v_pk_max_f16 v160, v160, v161
	v_pk_max_f16 v162, v162, v163
	v_mfma_f32_32x32x16_f16 a[192:207], v[38:41], v[118:121], a[192:207]
	ds_read_b128 v[78:81], v208 offset:24576
	v_cndmask_b32_e64 v114, v1, v148, s[36:37]
	s_mov_b64 vcc, s[38:39]
	v_cndmask_b32_sdwa v114, v1, v148, vcc dst_sel:WORD_1 dst_unused:UNUSED_PRESERVE src0_sel:WORD_1 src1_sel:WORD_1
	v_cndmask_b32_e64 v115, v1, v150, s[40:41]
	s_mov_b64 vcc, s[42:43]
	v_cndmask_b32_sdwa v115, v1, v150, vcc dst_sel:WORD_1 dst_unused:UNUSED_PRESERVE src0_sel:WORD_1 src1_sel:WORD_1
	v_mfma_f32_32x32x16_f16 a[64:79], v[18:21], v[106:109], a[64:79]
	ds_read_b128 v[102:105], v208 offset:28672
	v_cndmask_b32_e64 v116, v1, v152, s[44:45]
	s_mov_b64 vcc, s[46:47]
	v_cndmask_b32_sdwa v116, v1, v152, vcc dst_sel:WORD_1 dst_unused:UNUSED_PRESERVE src0_sel:WORD_1 src1_sel:WORD_1
	v_cndmask_b32_e64 v117, v1, v154, s[48:49]
	s_mov_b64 vcc, s[50:51]
	v_cndmask_b32_sdwa v117, v1, v154, vcc dst_sel:WORD_1 dst_unused:UNUSED_PRESERVE src0_sel:WORD_1 src1_sel:WORD_1
	v_mfma_f32_32x32x16_f16 a[176:191], v[38:41], v[106:109], a[176:191]
	v_cndmask_b32_e64 v110, v138, v156, s[4:5]
	s_mov_b64 vcc, s[6:7]
	v_cndmask_b32_sdwa v110, v138, v156, vcc dst_sel:WORD_1 dst_unused:UNUSED_PRESERVE src0_sel:WORD_1 src1_sel:WORD_1
	v_cndmask_b32_e64 v111, v138, v158, s[8:9]
	s_mov_b64 vcc, s[10:11]
	v_cndmask_b32_sdwa v111, v138, v158, vcc dst_sel:WORD_1 dst_unused:UNUSED_PRESERVE src0_sel:WORD_1 src1_sel:WORD_1
	v_mfma_f32_32x32x16_f16 a[112:127], v[18:21], v[98:101], a[112:127]
	v_cndmask_b32_e64 v112, v138, v160, s[12:13]
	s_mov_b64 vcc, s[14:15]
	v_cndmask_b32_sdwa v112, v138, v160, vcc dst_sel:WORD_1 dst_unused:UNUSED_PRESERVE src0_sel:WORD_1 src1_sel:WORD_1
	v_cndmask_b32_e64 v113, v138, v162, s[16:17]
	s_mov_b64 vcc, s[18:19]
	v_cndmask_b32_sdwa v113, v138, v162, vcc dst_sel:WORD_1 dst_unused:UNUSED_PRESERVE src0_sel:WORD_1 src1_sel:WORD_1
	v_mfma_f32_32x32x16_f16 a[160:175], v[38:41], v[98:101], a[160:175]
	v_pk_add_f16 v148, v115, v114
	v_pk_add_f16 v149, v116, v117
	v_mfma_f32_32x32x16_f16 a[128:143], v[18:21], v[94:97], a[128:143]
	v_pk_add_f16 v150, v111, v110
	v_pk_add_f16 v151, v112, v113
	v_mfma_f32_32x32x16_f16 a[144:159], v[38:41], v[94:97], a[144:159]
	v_pk_add_f16 v148, v148, v149
	v_pk_add_f16 v150, v150, v151
	v_mfma_f32_32x32x16_f16 a[80:95], v[18:21], v[86:89], a[80:95]
	v_dot2c_f32_f16_e32 v134, 0x3c003c00, v148
	v_dot2c_f32_f16_e32 v135, 0x3c003c00, v150
	v_mfma_f32_32x32x16_f16 a[96:111], v[38:41], v[86:89], a[96:111]
	s_waitcnt lgkmcnt(0)
	v_mfma_f32_32x32x16_f16 a[0:15], v[114:117], v[50:53], a[0:15]
	s_load_dwordx16 s[36:51], s[0:1], 0xfc0
	s_load_dwordx16 s[4:19], s[0:1], 0x8fc0
	ds_read_b128 v[46:49], v142 offset:2016
	ds_read_b128 v[42:45], v142 offset:4064
	v_mfma_f32_32x32x16_f16 a[240:255], v[110:113], v[50:53], a[240:255]
	ds_read_b128 v[74:77], v209
	v_pk_mul_f16 v148, v90, v136
	v_pk_mul_f16 v149, v82, v137
	v_pk_mul_f16 v150, v91, v136
	v_pk_mul_f16 v151, v83, v137
	v_mfma_f32_32x32x16_f16 a[16:31], v[114:117], v[54:57], a[16:31]
	ds_read_b128 v[126:129], v209 offset:4096
	v_pk_mul_f16 v152, v92, v136
	v_pk_mul_f16 v153, v84, v137
	v_pk_mul_f16 v154, v93, v136
	v_pk_mul_f16 v155, v85, v137
	v_mfma_f32_32x32x16_f16 a[224:239], v[110:113], v[54:57], a[224:239]
	ds_read_b128 v[122:125], v209 offset:8192
	v_pk_mul_f16 v156, v90, v140
	v_pk_mul_f16 v157, v82, v139
	v_pk_mul_f16 v158, v91, v140
	v_pk_mul_f16 v159, v83, v139
	v_mfma_f32_32x32x16_f16 a[32:47], v[114:117], v[58:61], a[32:47]
	ds_read_b128 v[118:121], v209 offset:12288
	v_pk_mul_f16 v160, v92, v140
	v_pk_mul_f16 v161, v84, v139
	v_pk_mul_f16 v162, v93, v140
	v_pk_mul_f16 v163, v85, v139
	v_mfma_f32_32x32x16_f16 a[208:223], v[110:113], v[58:61], a[208:223]
	ds_read_b128 v[106:109], v209 offset:16384
	v_pk_max_f16 v148, v148, v149
	v_pk_max_f16 v150, v150, v151
	v_pk_max_f16 v152, v152, v153
	v_pk_max_f16 v154, v154, v155
	v_mfma_f32_32x32x16_f16 a[48:63], v[114:117], v[62:65], a[48:63]
	ds_read_b128 v[98:101], v209 offset:20480
	v_pk_max_f16 v156, v156, v157
	v_pk_max_f16 v158, v158, v159
	v_pk_max_f16 v160, v160, v161
	v_pk_max_f16 v162, v162, v163
	v_mfma_f32_32x32x16_f16 a[192:207], v[110:113], v[62:65], a[192:207]
	ds_read_b128 v[94:97], v209 offset:24576
	v_cndmask_b32_e64 v18, v1, v148, s[68:69]
	s_mov_b64 vcc, s[70:71]
	v_cndmask_b32_sdwa v18, v1, v148, vcc dst_sel:WORD_1 dst_unused:UNUSED_PRESERVE src0_sel:WORD_1 src1_sel:WORD_1
	v_cndmask_b32_e64 v19, v1, v150, s[72:73]
	s_mov_b64 vcc, s[74:75]
	v_cndmask_b32_sdwa v19, v1, v150, vcc dst_sel:WORD_1 dst_unused:UNUSED_PRESERVE src0_sel:WORD_1 src1_sel:WORD_1
	v_mfma_f32_32x32x16_f16 a[64:79], v[114:117], v[66:69], a[64:79]
	ds_read_b128 v[86:89], v209 offset:28672
	v_cndmask_b32_e64 v20, v1, v152, s[76:77]
	s_mov_b64 vcc, s[78:79]
	v_cndmask_b32_sdwa v20, v1, v152, vcc dst_sel:WORD_1 dst_unused:UNUSED_PRESERVE src0_sel:WORD_1 src1_sel:WORD_1
	v_cndmask_b32_e64 v21, v1, v154, s[80:81]
	s_mov_b64 vcc, s[82:83]
	v_cndmask_b32_sdwa v21, v1, v154, vcc dst_sel:WORD_1 dst_unused:UNUSED_PRESERVE src0_sel:WORD_1 src1_sel:WORD_1
	v_mfma_f32_32x32x16_f16 a[176:191], v[110:113], v[66:69], a[176:191]
	v_cndmask_b32_e64 v38, v138, v156, s[52:53]
	s_mov_b64 vcc, s[54:55]
	v_cndmask_b32_sdwa v38, v138, v156, vcc dst_sel:WORD_1 dst_unused:UNUSED_PRESERVE src0_sel:WORD_1 src1_sel:WORD_1
	v_cndmask_b32_e64 v39, v138, v158, s[56:57]
	s_mov_b64 vcc, s[58:59]
	v_cndmask_b32_sdwa v39, v138, v158, vcc dst_sel:WORD_1 dst_unused:UNUSED_PRESERVE src0_sel:WORD_1 src1_sel:WORD_1
	v_mfma_f32_32x32x16_f16 a[112:127], v[114:117], v[70:73], a[112:127]
	v_cndmask_b32_e64 v40, v138, v160, s[60:61]
	s_mov_b64 vcc, s[62:63]
	v_cndmask_b32_sdwa v40, v138, v160, vcc dst_sel:WORD_1 dst_unused:UNUSED_PRESERVE src0_sel:WORD_1 src1_sel:WORD_1
	v_cndmask_b32_e64 v41, v138, v162, s[64:65]
	s_mov_b64 vcc, s[66:67]
	v_cndmask_b32_sdwa v41, v138, v162, vcc dst_sel:WORD_1 dst_unused:UNUSED_PRESERVE src0_sel:WORD_1 src1_sel:WORD_1
	v_mfma_f32_32x32x16_f16 a[160:175], v[110:113], v[70:73], a[160:175]
	v_pk_add_f16 v148, v19, v18
	v_pk_add_f16 v149, v20, v21
	v_mfma_f32_32x32x16_f16 a[128:143], v[114:117], v[78:81], a[128:143]
	v_pk_add_f16 v150, v39, v38
	v_pk_add_f16 v151, v40, v41
	v_mfma_f32_32x32x16_f16 a[144:159], v[110:113], v[78:81], a[144:159]
	v_pk_add_f16 v148, v148, v149
	v_pk_add_f16 v150, v150, v151
	v_mfma_f32_32x32x16_f16 a[80:95], v[114:117], v[102:105], a[80:95]
	v_dot2c_f32_f16_e32 v134, 0x3c003c00, v148
	v_dot2c_f32_f16_e32 v135, 0x3c003c00, v150
	v_mfma_f32_32x32x16_f16 a[96:111], v[110:113], v[102:105], a[96:111]
	s_waitcnt lgkmcnt(0)
	v_mfma_f32_32x32x16_f16 a[0:15], v[18:21], v[74:77], a[0:15]
	v_mfma_f32_32x32x16_f16 a[240:255], v[38:41], v[74:77], a[240:255]
	ds_read_b128 v[50:53], v210
	v_pk_mul_f16 v148, v46, v136
	v_pk_mul_f16 v149, v42, v137
	v_pk_mul_f16 v150, v47, v136
	v_pk_mul_f16 v151, v43, v137
	v_mfma_f32_32x32x16_f16 a[16:31], v[18:21], v[126:129], a[16:31]
	ds_read_b128 v[54:57], v210 offset:4096
	v_pk_mul_f16 v152, v48, v136
	v_pk_mul_f16 v153, v44, v137
	v_pk_mul_f16 v154, v49, v136
	v_pk_mul_f16 v155, v45, v137
	v_mfma_f32_32x32x16_f16 a[224:239], v[38:41], v[126:129], a[224:239]
	ds_read_b128 v[58:61], v210 offset:8192
	v_pk_mul_f16 v156, v46, v140
	v_pk_mul_f16 v157, v42, v139
	v_pk_mul_f16 v158, v47, v140
	v_pk_mul_f16 v159, v43, v139
	v_mfma_f32_32x32x16_f16 a[32:47], v[18:21], v[122:125], a[32:47]
	ds_read_b128 v[62:65], v210 offset:12288
	v_pk_mul_f16 v160, v48, v140
	v_pk_mul_f16 v161, v44, v139
	v_pk_mul_f16 v162, v49, v140
	v_pk_mul_f16 v163, v45, v139
	v_mfma_f32_32x32x16_f16 a[208:223], v[38:41], v[122:125], a[208:223]
	ds_read_b128 v[66:69], v210 offset:16384
	v_pk_max_f16 v148, v148, v149
	v_pk_max_f16 v150, v150, v151
	v_pk_max_f16 v152, v152, v153
	v_pk_max_f16 v154, v154, v155
	v_mfma_f32_32x32x16_f16 a[48:63], v[18:21], v[118:121], a[48:63]
	ds_read_b128 v[70:73], v210 offset:20480
	v_pk_max_f16 v156, v156, v157
	v_pk_max_f16 v158, v158, v159
	v_pk_max_f16 v160, v160, v161
	v_pk_max_f16 v162, v162, v163
	v_mfma_f32_32x32x16_f16 a[192:207], v[38:41], v[118:121], a[192:207]
	ds_read_b128 v[78:81], v210 offset:24576
	v_cndmask_b32_e64 v114, v1, v148, s[36:37]
	s_mov_b64 vcc, s[38:39]
	v_cndmask_b32_sdwa v114, v1, v148, vcc dst_sel:WORD_1 dst_unused:UNUSED_PRESERVE src0_sel:WORD_1 src1_sel:WORD_1
	v_cndmask_b32_e64 v115, v1, v150, s[40:41]
	s_mov_b64 vcc, s[42:43]
	v_cndmask_b32_sdwa v115, v1, v150, vcc dst_sel:WORD_1 dst_unused:UNUSED_PRESERVE src0_sel:WORD_1 src1_sel:WORD_1
	v_mfma_f32_32x32x16_f16 a[64:79], v[18:21], v[106:109], a[64:79]
	ds_read_b128 v[102:105], v210 offset:28672
	v_cndmask_b32_e64 v116, v1, v152, s[44:45]
	s_mov_b64 vcc, s[46:47]
	v_cndmask_b32_sdwa v116, v1, v152, vcc dst_sel:WORD_1 dst_unused:UNUSED_PRESERVE src0_sel:WORD_1 src1_sel:WORD_1
	v_cndmask_b32_e64 v117, v1, v154, s[48:49]
	s_mov_b64 vcc, s[50:51]
	v_cndmask_b32_sdwa v117, v1, v154, vcc dst_sel:WORD_1 dst_unused:UNUSED_PRESERVE src0_sel:WORD_1 src1_sel:WORD_1
	v_mfma_f32_32x32x16_f16 a[176:191], v[38:41], v[106:109], a[176:191]
	v_cndmask_b32_e64 v110, v138, v156, s[4:5]
	s_mov_b64 vcc, s[6:7]
	v_cndmask_b32_sdwa v110, v138, v156, vcc dst_sel:WORD_1 dst_unused:UNUSED_PRESERVE src0_sel:WORD_1 src1_sel:WORD_1
	v_cndmask_b32_e64 v111, v138, v158, s[8:9]
	s_mov_b64 vcc, s[10:11]
	v_cndmask_b32_sdwa v111, v138, v158, vcc dst_sel:WORD_1 dst_unused:UNUSED_PRESERVE src0_sel:WORD_1 src1_sel:WORD_1
	v_mfma_f32_32x32x16_f16 a[112:127], v[18:21], v[98:101], a[112:127]
	v_cndmask_b32_e64 v112, v138, v160, s[12:13]
	s_mov_b64 vcc, s[14:15]
	v_cndmask_b32_sdwa v112, v138, v160, vcc dst_sel:WORD_1 dst_unused:UNUSED_PRESERVE src0_sel:WORD_1 src1_sel:WORD_1
	v_cndmask_b32_e64 v113, v138, v162, s[16:17]
	s_mov_b64 vcc, s[18:19]
	v_cndmask_b32_sdwa v113, v138, v162, vcc dst_sel:WORD_1 dst_unused:UNUSED_PRESERVE src0_sel:WORD_1 src1_sel:WORD_1
	v_mfma_f32_32x32x16_f16 a[160:175], v[38:41], v[98:101], a[160:175]
	v_pk_add_f16 v148, v115, v114
	v_pk_add_f16 v149, v116, v117
	v_mfma_f32_32x32x16_f16 a[128:143], v[18:21], v[94:97], a[128:143]
	v_pk_add_f16 v150, v111, v110
	v_pk_add_f16 v151, v112, v113
	v_mfma_f32_32x32x16_f16 a[144:159], v[38:41], v[94:97], a[144:159]
	v_pk_add_f16 v148, v148, v149
	v_pk_add_f16 v150, v150, v151
	v_mfma_f32_32x32x16_f16 a[80:95], v[18:21], v[86:89], a[80:95]
	v_dot2c_f32_f16_e32 v134, 0x3c003c00, v148
	v_dot2c_f32_f16_e32 v135, 0x3c003c00, v150
	v_mfma_f32_32x32x16_f16 a[96:111], v[38:41], v[86:89], a[96:111]
	s_waitcnt lgkmcnt(0)
	v_mfma_f32_32x32x16_f16 a[0:15], v[114:117], v[50:53], a[0:15]
	v_mfma_f32_32x32x16_f16 a[240:255], v[110:113], v[50:53], a[240:255]
	v_mfma_f32_32x32x16_f16 a[16:31], v[114:117], v[54:57], a[16:31]
	v_mfma_f32_32x32x16_f16 a[224:239], v[110:113], v[54:57], a[224:239]
	v_mfma_f32_32x32x16_f16 a[32:47], v[114:117], v[58:61], a[32:47]
	v_mfma_f32_32x32x16_f16 a[208:223], v[110:113], v[58:61], a[208:223]
	v_mfma_f32_32x32x16_f16 a[48:63], v[114:117], v[62:65], a[48:63]
	v_mfma_f32_32x32x16_f16 a[192:207], v[110:113], v[62:65], a[192:207]
	v_mfma_f32_32x32x16_f16 a[64:79], v[114:117], v[66:69], a[64:79]
	v_mfma_f32_32x32x16_f16 a[176:191], v[110:113], v[66:69], a[176:191]
	v_mfma_f32_32x32x16_f16 a[112:127], v[114:117], v[70:73], a[112:127]
	v_mfma_f32_32x32x16_f16 a[160:175], v[110:113], v[70:73], a[160:175]
	v_mfma_f32_32x32x16_f16 a[128:143], v[114:117], v[78:81], a[128:143]
	v_mfma_f32_32x32x16_f16 a[144:159], v[110:113], v[78:81], a[144:159]
	v_mfma_f32_32x32x16_f16 a[80:95], v[114:117], v[102:105], a[80:95]
	v_mfma_f32_32x32x16_f16 a[96:111], v[110:113], v[102:105], a[96:111]
	v_readfirstlane_b32 s1, v0
	s_and_b32 s0, s3, 0xffffff00
	s_andn2_b32 s1, s1, 63
	s_add_i32 s4, s1, s0
	s_lshl_b32 s0, s2, 13
	s_and_b32 s6, s0, 0xe000
	s_ashr_i32 s5, s4, 31
	s_add_u32 s0, s4, s6
	s_addc_u32 s1, s5, 0
	s_lshl_b64 s[2:3], s[0:1], 9
	v_lshrrev_b32_e32 v0, 3, v132
	s_add_u32 s2, s22, s2
	v_and_b32_e32 v3, 12, v0
	s_addc_u32 s3, s23, s3
	v_lshlrev_b32_e32 v0, 9, v3
	v_mov_b32_e32 v1, 0
	v_lshl_add_u64 v[4:5], s[2:3], 0, v[0:1]
	v_lshlrev_b32_e32 v0, 4, v132
	v_and_b32_e32 v0, 0x1f0, v0
	v_lshl_add_u64 v[4:5], v[4:5], 0, v[0:1]
	v_accvgpr_read_b32 v6, a0
	v_accvgpr_read_b32 v7, a16
	v_accvgpr_read_b32 v8, a32
	v_max3_f32 v0, |v6|, |v7|, |v8|
	v_accvgpr_read_b32 v9, a48
	v_accvgpr_read_b32 v14, a64
	v_max3_f32 v0, |v0|, |v9|, |v14|
	v_accvgpr_read_b32 v15, a112
	v_accvgpr_read_b32 v16, a128
	v_max3_f32 v0, |v0|, |v15|, |v16|
	v_accvgpr_read_b32 v17, a80
	v_max3_f32 v10, |v0|, |v17|, |v17|
	v_accvgpr_read_b32 v18, a1
	v_accvgpr_read_b32 v19, a17
	v_accvgpr_read_b32 v20, a33
	v_max3_f32 v0, |v18|, |v19|, |v20|
	v_accvgpr_read_b32 v21, a49
	v_accvgpr_read_b32 v22, a65
	v_max3_f32 v0, |v0|, |v21|, |v22|
	v_accvgpr_read_b32 v23, a113
	v_accvgpr_read_b32 v24, a129
	v_max3_f32 v0, |v0|, |v23|, |v24|
	v_accvgpr_read_b32 v25, a81
	v_max3_f32 v11, |v0|, |v25|, |v25|
	v_accvgpr_read_b32 v26, a2
	v_accvgpr_read_b32 v27, a18
	v_accvgpr_read_b32 v28, a34
	v_max3_f32 v0, |v26|, |v27|, |v28|
	v_accvgpr_read_b32 v29, a50
	v_accvgpr_read_b32 v30, a66
	v_max3_f32 v0, |v0|, |v29|, |v30|
	v_accvgpr_read_b32 v31, a114
	v_accvgpr_read_b32 v32, a130
	v_max3_f32 v0, |v0|, |v31|, |v32|
	v_accvgpr_read_b32 v33, a82
	v_max3_f32 v12, |v0|, |v33|, |v33|
	v_accvgpr_read_b32 v34, a3
	v_accvgpr_read_b32 v35, a19
	v_accvgpr_read_b32 v36, a35
	v_max3_f32 v0, |v34|, |v35|, |v36|
	v_accvgpr_read_b32 v37, a51
	v_accvgpr_read_b32 v38, a67
	v_max3_f32 v0, |v0|, |v37|, |v38|
	v_accvgpr_read_b32 v39, a115
	v_accvgpr_read_b32 v40, a131
	v_max3_f32 v0, |v0|, |v39|, |v40|
	v_accvgpr_read_b32 v41, a83
	v_max3_f32 v13, |v0|, |v41|, |v41|
	v_lshlrev_b32_e32 v0, 2, v3
	s_nop 1
	v_max_f32_dpp v10, v10, v10 quad_perm:[1,0,3,2] row_mask:0xf bank_mask:0xf
	v_max_f32_dpp v11, v11, v11 quad_perm:[1,0,3,2] row_mask:0xf bank_mask:0xf
	v_max_f32_dpp v12, v12, v12 quad_perm:[1,0,3,2] row_mask:0xf bank_mask:0xf
	v_max_f32_dpp v13, v13, v13 quad_perm:[1,0,3,2] row_mask:0xf bank_mask:0xf
	v_max_f32_dpp v10, v10, v10 quad_perm:[2,3,0,1] row_mask:0xf bank_mask:0xf
	v_max_f32_dpp v11, v11, v11 quad_perm:[2,3,0,1] row_mask:0xf bank_mask:0xf
	v_max_f32_dpp v12, v12, v12 quad_perm:[2,3,0,1] row_mask:0xf bank_mask:0xf
	v_max_f32_dpp v13, v13, v13 quad_perm:[2,3,0,1] row_mask:0xf bank_mask:0xf
	v_max_f32_dpp v10, v10, v10 row_half_mirror row_mask:0xf bank_mask:0xf
	v_max_f32_dpp v11, v11, v11 row_half_mirror row_mask:0xf bank_mask:0xf
	v_max_f32_dpp v12, v12, v12 row_half_mirror row_mask:0xf bank_mask:0xf
	v_max_f32_dpp v13, v13, v13 row_half_mirror row_mask:0xf bank_mask:0xf
	v_max_f32_dpp v10, v10, v10 row_mirror row_mask:0xf bank_mask:0xf
	v_max_f32_dpp v11, v11, v11 row_mirror row_mask:0xf bank_mask:0xf
	v_max_f32_dpp v12, v12, v12 row_mirror row_mask:0xf bank_mask:0xf
	v_max_f32_dpp v13, v13, v13 row_mirror row_mask:0xf bank_mask:0xf
	s_nop 0
	ds_swizzle_b32 v232, v10 offset:swizzle(SWAP,16)
	ds_swizzle_b32 v233, v12 offset:swizzle(SWAP,16)
	ds_swizzle_b32 v234, v11 offset:swizzle(SWAP,16)
	ds_swizzle_b32 v235, v13 offset:swizzle(SWAP,16)
	s_waitcnt lgkmcnt(0)
	v_max_f32_e32 v10, v10, v232
	v_rcp_f32_e32 v42, v10
	v_cmp_lt_f32_e32 vcc, 0, v10
	s_waitcnt lgkmcnt(0)
	v_max_f32_e32 v12, v12, v233
	s_waitcnt lgkmcnt(0)
	v_max_f32_e32 v11, v11, v234
	s_lshl_b32 s2, s6, 2
	v_cndmask_b32_e32 v3, 0, v42, vcc
	v_pk_mul_f32 v[224:225], v[6:7], v[2:3] op_sel:[0,1] op_sel_hi:[1,1]
	v_pk_mul_f32 v[226:227], v[8:9], v[2:3] op_sel:[0,1] op_sel_hi:[1,1]
	v_cvt_pknorm_i16_f32 v6, v224, v225
	v_cvt_pknorm_i16_f32 v7, v226, v227
	v_pk_mul_f32 v[228:229], v[14:15], v[2:3] op_sel:[0,1] op_sel_hi:[1,1]
	v_rcp_f32_e32 v14, v11
	v_cvt_pknorm_i16_f32 v8, v228, v229
	v_pk_mul_f32 v[230:231], v[16:17], v[2:3] op_sel:[0,1] op_sel_hi:[1,1]
	v_cmp_lt_f32_e32 vcc, 0, v11
	v_cvt_pknorm_i16_f32 v9, v230, v231
	global_store_dwordx4 v[4:5], v[6:9], off sc0 sc1
	s_add_u32 s6, s24, s2
	v_cndmask_b32_e32 v3, 0, v14, vcc
	v_pk_mul_f32 v[224:225], v[18:19], v[2:3] op_sel:[0,1] op_sel_hi:[1,1]
	v_pk_mul_f32 v[226:227], v[20:21], v[2:3] op_sel:[0,1] op_sel_hi:[1,1]
	v_cvt_pknorm_i16_f32 v6, v224, v225
	v_cvt_pknorm_i16_f32 v7, v226, v227
	v_pk_mul_f32 v[228:229], v[22:23], v[2:3] op_sel:[0,1] op_sel_hi:[1,1]
	v_pk_mul_f32 v[230:231], v[24:25], v[2:3] op_sel:[0,1] op_sel_hi:[1,1]
	v_cvt_pknorm_i16_f32 v8, v228, v229
	v_cvt_pknorm_i16_f32 v9, v230, v231
	v_rcp_f32_e32 v3, v12
	s_addc_u32 s7, s25, 0
	s_lshl_b64 s[2:3], s[4:5], 2
	s_mov_b64 s[4:5], 0x200
	s_add_u32 s2, s6, s2
	v_lshl_add_u64 v[14:15], v[4:5], 0, s[4:5]
	s_mov_b32 s4, 0x38000100
	v_cmp_lt_f32_e32 vcc, 0, v12
	s_addc_u32 s3, s7, s3
	global_store_dwordx4 v[14:15], v[6:9], off sc0 sc1
	s_nop 1
	v_pk_mul_f32 v[6:7], v[10:11], s[4:5] op_sel_hi:[1,0]
	v_cndmask_b32_e32 v3, 0, v3, vcc
	global_store_dwordx2 v0, v[6:7], s[2:3]
	v_pk_mul_f32 v[224:225], v[26:27], v[2:3] op_sel:[0,1] op_sel_hi:[1,1]
	v_pk_mul_f32 v[226:227], v[28:29], v[2:3] op_sel:[0,1] op_sel_hi:[1,1]
	v_cvt_pknorm_i16_f32 v6, v224, v225
	v_cvt_pknorm_i16_f32 v7, v226, v227
	v_pk_mul_f32 v[228:229], v[30:31], v[2:3] op_sel:[0,1] op_sel_hi:[1,1]
	v_pk_mul_f32 v[230:231], v[32:33], v[2:3] op_sel:[0,1] op_sel_hi:[1,1]
	v_cvt_pknorm_i16_f32 v8, v228, v229
	s_waitcnt lgkmcnt(0)
	v_max_f32_e32 v13, v13, v235
	v_cvt_pknorm_i16_f32 v9, v230, v231
	v_rcp_f32_e32 v3, v13
	v_cmp_lt_f32_e32 vcc, 0, v13
	s_mov_b64 s[6:7], 0x400
	v_lshl_add_u64 v[10:11], v[4:5], 0, s[6:7]
	v_cndmask_b32_e32 v3, 0, v3, vcc
	global_store_dwordx4 v[10:11], v[6:9], off sc0 sc1
	v_pk_mul_f32 v[224:225], v[34:35], v[2:3] op_sel:[0,1] op_sel_hi:[1,1]
	v_pk_mul_f32 v[226:227], v[36:37], v[2:3] op_sel:[0,1] op_sel_hi:[1,1]
	v_cvt_pknorm_i16_f32 v6, v224, v225
	v_cvt_pknorm_i16_f32 v7, v226, v227
	v_pk_mul_f32 v[228:229], v[38:39], v[2:3] op_sel:[0,1] op_sel_hi:[1,1]
	v_pk_mul_f32 v[230:231], v[40:41], v[2:3] op_sel:[0,1] op_sel_hi:[1,1]
	v_cvt_pknorm_i16_f32 v8, v228, v229
	s_mov_b64 s[6:7], 0x600
	v_cvt_pknorm_i16_f32 v9, v230, v231
	v_lshl_add_u64 v[10:11], v[4:5], 0, s[6:7]
	global_store_dwordx4 v[10:11], v[6:9], off sc0 sc1
	s_nop 1
	v_pk_mul_f32 v[6:7], v[12:13], s[4:5] op_sel_hi:[1,0]
	v_lshlrev_b32_e32 v2, 2, v132
	global_store_dwordx2 v0, v[6:7], s[2:3] offset:8
	v_accvgpr_read_b32 v42, a4
	v_accvgpr_read_b32 v6, a20
	v_accvgpr_read_b32 v7, a36
	v_max3_f32 v8, |v42|, |v6|, |v7|
	v_accvgpr_read_b32 v9, a52
	v_accvgpr_read_b32 v14, a68
	v_max3_f32 v8, |v8|, |v9|, |v14|
	v_accvgpr_read_b32 v15, a116
	v_accvgpr_read_b32 v16, a132
	v_max3_f32 v8, |v8|, |v15|, |v16|
	v_accvgpr_read_b32 v10, a84
	v_accvgpr_read_b32 v43, a5
	v_accvgpr_read_b32 v17, a84
	v_max3_f32 v8, |v8|, |v17|, |v10|
	v_accvgpr_read_b32 v19, a21
	v_accvgpr_read_b32 v20, a37
	v_max3_f32 v10, |v43|, |v19|, |v20|
	v_accvgpr_read_b32 v21, a53
	v_accvgpr_read_b32 v22, a69
	v_max3_f32 v10, |v10|, |v21|, |v22|
	v_accvgpr_read_b32 v23, a117
	v_accvgpr_read_b32 v24, a133
	v_max3_f32 v10, |v10|, |v23|, |v24|
	v_accvgpr_read_b32 v44, a6
	v_accvgpr_read_b32 v25, a85
	v_max3_f32 v11, |v10|, |v25|, |v25|
	v_accvgpr_read_b32 v27, a22
	v_accvgpr_read_b32 v28, a38
	v_max3_f32 v10, |v44|, |v27|, |v28|
	v_accvgpr_read_b32 v29, a54
	v_accvgpr_read_b32 v30, a70
	v_max3_f32 v10, |v10|, |v29|, |v30|
	v_accvgpr_read_b32 v31, a118
	v_accvgpr_read_b32 v32, a134
	v_max3_f32 v10, |v10|, |v31|, |v32|
	v_accvgpr_read_b32 v45, a7
	v_accvgpr_read_b32 v33, a86
	v_max3_f32 v12, |v10|, |v33|, |v33|
	v_accvgpr_read_b32 v35, a23
	v_accvgpr_read_b32 v36, a39
	v_max3_f32 v10, |v45|, |v35|, |v36|
	v_accvgpr_read_b32 v37, a55
	v_accvgpr_read_b32 v38, a71
	v_max3_f32 v10, |v10|, |v37|, |v38|
	v_accvgpr_read_b32 v39, a119
	v_accvgpr_read_b32 v40, a135
	v_max3_f32 v10, |v10|, |v39|, |v40|
	v_accvgpr_read_b32 v41, a87
	v_max3_f32 v13, |v10|, |v41|, |v41|
	v_mov_b32_e32 v3, v42
	s_nop 1
	v_max_f32_dpp v8, v8, v8 quad_perm:[1,0,3,2] row_mask:0xf bank_mask:0xf
	v_max_f32_dpp v11, v11, v11 quad_perm:[1,0,3,2] row_mask:0xf bank_mask:0xf
	v_max_f32_dpp v12, v12, v12 quad_perm:[1,0,3,2] row_mask:0xf bank_mask:0xf
	v_max_f32_dpp v13, v13, v13 quad_perm:[1,0,3,2] row_mask:0xf bank_mask:0xf
	v_max_f32_dpp v8, v8, v8 quad_perm:[2,3,0,1] row_mask:0xf bank_mask:0xf
	v_max_f32_dpp v11, v11, v11 quad_perm:[2,3,0,1] row_mask:0xf bank_mask:0xf
	v_max_f32_dpp v12, v12, v12 quad_perm:[2,3,0,1] row_mask:0xf bank_mask:0xf
	v_max_f32_dpp v13, v13, v13 quad_perm:[2,3,0,1] row_mask:0xf bank_mask:0xf
	v_max_f32_dpp v8, v8, v8 row_half_mirror row_mask:0xf bank_mask:0xf
	v_max_f32_dpp v11, v11, v11 row_half_mirror row_mask:0xf bank_mask:0xf
	v_max_f32_dpp v12, v12, v12 row_half_mirror row_mask:0xf bank_mask:0xf
	v_max_f32_dpp v13, v13, v13 row_half_mirror row_mask:0xf bank_mask:0xf
	v_max_f32_dpp v8, v8, v8 row_mirror row_mask:0xf bank_mask:0xf
	v_max_f32_dpp v11, v11, v11 row_mirror row_mask:0xf bank_mask:0xf
	v_max_f32_dpp v12, v12, v12 row_mirror row_mask:0xf bank_mask:0xf
	v_max_f32_dpp v13, v13, v13 row_mirror row_mask:0xf bank_mask:0xf
	s_nop 0
	ds_swizzle_b32 v232, v8 offset:swizzle(SWAP,16)
	ds_swizzle_b32 v233, v11 offset:swizzle(SWAP,16)
	ds_swizzle_b32 v234, v12 offset:swizzle(SWAP,16)
	ds_swizzle_b32 v235, v13 offset:swizzle(SWAP,16)
	s_waitcnt lgkmcnt(0)
	v_max_f32_e32 v10, v8, v232
	v_rcp_f32_e32 v8, v10
	v_cmp_lt_f32_e32 vcc, 0, v10
	s_waitcnt lgkmcnt(0)
	v_max_f32_e32 v11, v11, v233
	v_mov_b32_e32 v18, v43
	s_mov_b64 s[6:7], 0x1000
	v_cndmask_b32_e32 v42, 0, v8, vcc
	v_mul_f32_e32 v3, v42, v3
	v_mul_f32_e32 v6, v42, v6
	v_cvt_pknorm_i16_f32 v6, v3, v6
	v_mul_f32_e32 v3, v42, v7
	v_mul_f32_e32 v7, v42, v9
	v_cvt_pknorm_i16_f32 v7, v3, v7
	v_pk_mul_f32 v[224:225], v[14:15], v[42:43] op_sel_hi:[1,0]
	v_pk_mul_f32 v[226:227], v[16:17], v[42:43] op_sel_hi:[1,0]
	v_cvt_pknorm_i16_f32 v8, v224, v225
	v_cvt_pknorm_i16_f32 v9, v226, v227
	v_rcp_f32_e32 v3, v11
	v_cmp_lt_f32_e32 vcc, 0, v11
	v_lshl_add_u64 v[14:15], v[4:5], 0, s[6:7]
	global_store_dwordx4 v[14:15], v[6:9], off sc0 sc1
	v_cndmask_b32_e32 v3, 0, v3, vcc
	v_pk_mul_f32 v[228:229], v[18:19], v[2:3] op_sel:[0,1] op_sel_hi:[1,1]
	v_pk_mul_f32 v[230:231], v[20:21], v[2:3] op_sel:[0,1] op_sel_hi:[1,1]
	v_cvt_pknorm_i16_f32 v6, v228, v229
	v_cvt_pknorm_i16_f32 v7, v230, v231
	v_pk_mul_f32 v[224:225], v[22:23], v[2:3] op_sel:[0,1] op_sel_hi:[1,1]
	v_pk_mul_f32 v[226:227], v[24:25], v[2:3] op_sel:[0,1] op_sel_hi:[1,1]
	v_cvt_pknorm_i16_f32 v8, v224, v225
	s_waitcnt lgkmcnt(0)
	v_max_f32_e32 v12, v12, v234
	v_cvt_pknorm_i16_f32 v9, v226, v227
	v_rcp_f32_e32 v3, v12
	s_mov_b64 s[6:7], 0x1200
	v_cmp_lt_f32_e32 vcc, 0, v12
	v_mov_b32_e32 v26, v44
	v_lshl_add_u64 v[14:15], v[4:5], 0, s[6:7]
	global_store_dwordx4 v[14:15], v[6:9], off sc0 sc1
	s_nop 1
	v_pk_mul_f32 v[6:7], v[10:11], s[4:5] op_sel_hi:[1,0]
	v_cndmask_b32_e32 v3, 0, v3, vcc
	global_store_dwordx2 v0, v[6:7], s[2:3] offset:32
	v_pk_mul_f32 v[228:229], v[26:27], v[2:3] op_sel:[0,1] op_sel_hi:[1,1]
	v_pk_mul_f32 v[230:231], v[28:29], v[2:3] op_sel:[0,1] op_sel_hi:[1,1]
	v_cvt_pknorm_i16_f32 v6, v228, v229
	v_cvt_pknorm_i16_f32 v7, v230, v231
	v_pk_mul_f32 v[224:225], v[30:31], v[2:3] op_sel:[0,1] op_sel_hi:[1,1]
	v_pk_mul_f32 v[226:227], v[32:33], v[2:3] op_sel:[0,1] op_sel_hi:[1,1]
	v_cvt_pknorm_i16_f32 v8, v224, v225
	s_waitcnt lgkmcnt(0)
	v_max_f32_e32 v13, v13, v235
	v_cvt_pknorm_i16_f32 v9, v226, v227
	v_rcp_f32_e32 v3, v13
	v_cmp_lt_f32_e32 vcc, 0, v13
	v_mov_b32_e32 v34, v45
	s_mov_b64 s[6:7], 0x1400
	v_cndmask_b32_e32 v3, 0, v3, vcc
	v_lshl_add_u64 v[10:11], v[4:5], 0, s[6:7]
	global_store_dwordx4 v[10:11], v[6:9], off sc0 sc1
	v_pk_mul_f32 v[228:229], v[34:35], v[2:3] op_sel:[0,1] op_sel_hi:[1,1]
	v_pk_mul_f32 v[230:231], v[36:37], v[2:3] op_sel:[0,1] op_sel_hi:[1,1]
	v_cvt_pknorm_i16_f32 v6, v228, v229
	v_cvt_pknorm_i16_f32 v7, v230, v231
	v_pk_mul_f32 v[224:225], v[38:39], v[2:3] op_sel:[0,1] op_sel_hi:[1,1]
	v_pk_mul_f32 v[226:227], v[40:41], v[2:3] op_sel:[0,1] op_sel_hi:[1,1]
	v_cvt_pknorm_i16_f32 v8, v224, v225
	s_mov_b64 s[6:7], 0x1600
	v_cvt_pknorm_i16_f32 v9, v226, v227
	v_lshl_add_u64 v[10:11], v[4:5], 0, s[6:7]
	global_store_dwordx4 v[10:11], v[6:9], off sc0 sc1
	s_nop 1
	v_pk_mul_f32 v[6:7], v[12:13], s[4:5] op_sel_hi:[1,0]
	v_accvgpr_read_b32 v46, a8
	v_accvgpr_read_b32 v47, a9
	v_accvgpr_read_b32 v48, a10
	v_accvgpr_read_b32 v49, a11
	v_accvgpr_read_b32 v50, a12
	v_accvgpr_read_b32 v51, a13
	v_accvgpr_read_b32 v52, a14
	v_accvgpr_read_b32 v53, a15
	global_store_dwordx2 v0, v[6:7], s[2:3] offset:40
	v_mov_b64_e32 v[42:43], v[46:47]
	v_accvgpr_read_b32 v6, a24
	v_accvgpr_read_b32 v7, a40
	v_max3_f32 v8, |v42|, |v6|, |v7|
	v_accvgpr_read_b32 v9, a56
	v_accvgpr_read_b32 v14, a72
	v_max3_f32 v8, |v8|, |v9|, |v14|
	v_accvgpr_read_b32 v15, a120
	v_accvgpr_read_b32 v16, a136
	v_max3_f32 v8, |v8|, |v15|, |v16|
	v_accvgpr_read_b32 v10, a88
	v_accvgpr_read_b32 v17, a88
	v_max3_f32 v8, |v8|, |v17|, |v10|
	v_accvgpr_read_b32 v19, a25
	v_accvgpr_read_b32 v20, a41
	v_max3_f32 v10, |v43|, |v19|, |v20|
	v_accvgpr_read_b32 v21, a57
	v_accvgpr_read_b32 v22, a73
	v_max3_f32 v10, |v10|, |v21|, |v22|
	v_accvgpr_read_b32 v23, a121
	v_accvgpr_read_b32 v24, a137
	v_max3_f32 v10, |v10|, |v23|, |v24|
	v_mov_b64_e32 v[44:45], v[48:49]
	v_accvgpr_read_b32 v25, a89
	v_max3_f32 v11, |v10|, |v25|, |v25|
	v_accvgpr_read_b32 v27, a26
	v_accvgpr_read_b32 v28, a42
	v_max3_f32 v10, |v44|, |v27|, |v28|
	v_accvgpr_read_b32 v29, a58
	v_accvgpr_read_b32 v30, a74
	v_max3_f32 v10, |v10|, |v29|, |v30|
	v_accvgpr_read_b32 v31, a122
	v_accvgpr_read_b32 v32, a138
	v_max3_f32 v10, |v10|, |v31|, |v32|
	v_accvgpr_read_b32 v33, a90
	v_max3_f32 v12, |v10|, |v33|, |v33|
	v_accvgpr_read_b32 v35, a27
	v_accvgpr_read_b32 v36, a43
	v_max3_f32 v10, |v45|, |v35|, |v36|
	v_accvgpr_read_b32 v37, a59
	v_accvgpr_read_b32 v38, a75
	v_max3_f32 v10, |v10|, |v37|, |v38|
	v_accvgpr_read_b32 v39, a123
	v_accvgpr_read_b32 v40, a139
	v_max3_f32 v10, |v10|, |v39|, |v40|
	v_accvgpr_read_b32 v41, a91
	v_max3_f32 v13, |v10|, |v41|, |v41|
	v_mov_b32_e32 v3, v42
	s_nop 1
	v_max_f32_dpp v8, v8, v8 quad_perm:[1,0,3,2] row_mask:0xf bank_mask:0xf
	v_max_f32_dpp v11, v11, v11 quad_perm:[1,0,3,2] row_mask:0xf bank_mask:0xf
	v_max_f32_dpp v12, v12, v12 quad_perm:[1,0,3,2] row_mask:0xf bank_mask:0xf
	v_max_f32_dpp v13, v13, v13 quad_perm:[1,0,3,2] row_mask:0xf bank_mask:0xf
	v_max_f32_dpp v8, v8, v8 quad_perm:[2,3,0,1] row_mask:0xf bank_mask:0xf
	v_max_f32_dpp v11, v11, v11 quad_perm:[2,3,0,1] row_mask:0xf bank_mask:0xf
	v_max_f32_dpp v12, v12, v12 quad_perm:[2,3,0,1] row_mask:0xf bank_mask:0xf
	v_max_f32_dpp v13, v13, v13 quad_perm:[2,3,0,1] row_mask:0xf bank_mask:0xf
	v_max_f32_dpp v8, v8, v8 row_half_mirror row_mask:0xf bank_mask:0xf
	v_max_f32_dpp v11, v11, v11 row_half_mirror row_mask:0xf bank_mask:0xf
	v_max_f32_dpp v12, v12, v12 row_half_mirror row_mask:0xf bank_mask:0xf
	v_max_f32_dpp v13, v13, v13 row_half_mirror row_mask:0xf bank_mask:0xf
	v_max_f32_dpp v8, v8, v8 row_mirror row_mask:0xf bank_mask:0xf
	v_max_f32_dpp v11, v11, v11 row_mirror row_mask:0xf bank_mask:0xf
	v_max_f32_dpp v12, v12, v12 row_mirror row_mask:0xf bank_mask:0xf
	v_max_f32_dpp v13, v13, v13 row_mirror row_mask:0xf bank_mask:0xf
	s_nop 0
	ds_swizzle_b32 v232, v8 offset:swizzle(SWAP,16)
	ds_swizzle_b32 v233, v11 offset:swizzle(SWAP,16)
	ds_swizzle_b32 v234, v12 offset:swizzle(SWAP,16)
	ds_swizzle_b32 v235, v13 offset:swizzle(SWAP,16)
	s_waitcnt lgkmcnt(0)
	v_max_f32_e32 v10, v8, v232
	v_rcp_f32_e32 v8, v10
	v_cmp_lt_f32_e32 vcc, 0, v10
	s_waitcnt lgkmcnt(0)
	v_max_f32_e32 v11, v11, v233
	v_mov_b32_e32 v18, v43
	s_mov_b64 s[6:7], 0x2000
	v_cndmask_b32_e32 v42, 0, v8, vcc
	v_mul_f32_e32 v3, v42, v3
	v_mul_f32_e32 v6, v42, v6
	v_cvt_pknorm_i16_f32 v6, v3, v6
	v_mul_f32_e32 v3, v42, v7
	v_mul_f32_e32 v7, v42, v9
	v_cvt_pknorm_i16_f32 v7, v3, v7
	v_pk_mul_f32 v[228:229], v[14:15], v[42:43] op_sel_hi:[1,0]
	v_pk_mul_f32 v[230:231], v[16:17], v[42:43] op_sel_hi:[1,0]
	v_cvt_pknorm_i16_f32 v8, v228, v229
	v_cvt_pknorm_i16_f32 v9, v230, v231
	v_rcp_f32_e32 v3, v11
	v_cmp_lt_f32_e32 vcc, 0, v11
	v_lshl_add_u64 v[14:15], v[4:5], 0, s[6:7]
	global_store_dwordx4 v[14:15], v[6:9], off sc0 sc1
	v_cndmask_b32_e32 v3, 0, v3, vcc
	v_pk_mul_f32 v[224:225], v[18:19], v[2:3] op_sel:[0,1] op_sel_hi:[1,1]
	v_pk_mul_f32 v[226:227], v[20:21], v[2:3] op_sel:[0,1] op_sel_hi:[1,1]
	v_cvt_pknorm_i16_f32 v6, v224, v225
	v_cvt_pknorm_i16_f32 v7, v226, v227
	v_pk_mul_f32 v[228:229], v[22:23], v[2:3] op_sel:[0,1] op_sel_hi:[1,1]
	v_pk_mul_f32 v[230:231], v[24:25], v[2:3] op_sel:[0,1] op_sel_hi:[1,1]
	v_cvt_pknorm_i16_f32 v8, v228, v229
	s_waitcnt lgkmcnt(0)
	v_max_f32_e32 v12, v12, v234
	v_cvt_pknorm_i16_f32 v9, v230, v231
	v_rcp_f32_e32 v3, v12
	s_mov_b64 s[6:7], 0x2200
	v_cmp_lt_f32_e32 vcc, 0, v12
	v_mov_b32_e32 v26, v44
	v_lshl_add_u64 v[14:15], v[4:5], 0, s[6:7]
	global_store_dwordx4 v[14:15], v[6:9], off sc0 sc1
	s_nop 1
	v_pk_mul_f32 v[6:7], v[10:11], s[4:5] op_sel_hi:[1,0]
	v_cndmask_b32_e32 v3, 0, v3, vcc
	global_store_dwordx2 v0, v[6:7], s[2:3] offset:64
	v_pk_mul_f32 v[224:225], v[26:27], v[2:3] op_sel:[0,1] op_sel_hi:[1,1]
	v_pk_mul_f32 v[226:227], v[28:29], v[2:3] op_sel:[0,1] op_sel_hi:[1,1]
	v_cvt_pknorm_i16_f32 v6, v224, v225
	v_cvt_pknorm_i16_f32 v7, v226, v227
	v_pk_mul_f32 v[228:229], v[30:31], v[2:3] op_sel:[0,1] op_sel_hi:[1,1]
	v_pk_mul_f32 v[230:231], v[32:33], v[2:3] op_sel:[0,1] op_sel_hi:[1,1]
	v_cvt_pknorm_i16_f32 v8, v228, v229
	s_waitcnt lgkmcnt(0)
	v_max_f32_e32 v13, v13, v235
	v_cvt_pknorm_i16_f32 v9, v230, v231
	v_rcp_f32_e32 v3, v13
	v_cmp_lt_f32_e32 vcc, 0, v13
	v_mov_b32_e32 v34, v45
	s_mov_b64 s[6:7], 0x2400
	v_cndmask_b32_e32 v3, 0, v3, vcc
	v_lshl_add_u64 v[10:11], v[4:5], 0, s[6:7]
	global_store_dwordx4 v[10:11], v[6:9], off sc0 sc1
	v_pk_mul_f32 v[224:225], v[34:35], v[2:3] op_sel:[0,1] op_sel_hi:[1,1]
	v_pk_mul_f32 v[226:227], v[36:37], v[2:3] op_sel:[0,1] op_sel_hi:[1,1]
	v_cvt_pknorm_i16_f32 v6, v224, v225
	v_cvt_pknorm_i16_f32 v7, v226, v227
	v_pk_mul_f32 v[228:229], v[38:39], v[2:3] op_sel:[0,1] op_sel_hi:[1,1]
	v_pk_mul_f32 v[230:231], v[40:41], v[2:3] op_sel:[0,1] op_sel_hi:[1,1]
	v_cvt_pknorm_i16_f32 v8, v228, v229
	s_mov_b64 s[6:7], 0x2600
	v_cvt_pknorm_i16_f32 v9, v230, v231
	v_lshl_add_u64 v[10:11], v[4:5], 0, s[6:7]
	global_store_dwordx4 v[10:11], v[6:9], off sc0 sc1
	s_nop 1
	v_pk_mul_f32 v[6:7], v[12:13], s[4:5] op_sel_hi:[1,0]
	v_mov_b64_e32 v[46:47], v[50:51]
	v_mov_b64_e32 v[48:49], v[52:53]
	global_store_dwordx2 v0, v[6:7], s[2:3] offset:72
	v_mov_b64_e32 v[32:33], v[46:47]
	v_accvgpr_read_b32 v6, a28
	v_accvgpr_read_b32 v7, a44
	v_max3_f32 v8, |v32|, |v6|, |v7|
	v_accvgpr_read_b32 v9, a60
	v_accvgpr_read_b32 v14, a76
	v_max3_f32 v8, |v8|, |v9|, |v14|
	v_accvgpr_read_b32 v15, a124
	v_accvgpr_read_b32 v16, a140
	v_max3_f32 v8, |v8|, |v15|, |v16|
	v_accvgpr_read_b32 v10, a92
	v_accvgpr_read_b32 v17, a92
	v_max3_f32 v8, |v8|, |v17|, |v10|
	v_accvgpr_read_b32 v19, a29
	v_accvgpr_read_b32 v20, a45
	v_max3_f32 v10, |v33|, |v19|, |v20|
	v_accvgpr_read_b32 v21, a61
	v_accvgpr_read_b32 v22, a77
	v_max3_f32 v10, |v10|, |v21|, |v22|
	v_accvgpr_read_b32 v23, a125
	v_accvgpr_read_b32 v24, a141
	v_max3_f32 v10, |v10|, |v23|, |v24|
	v_mov_b64_e32 v[34:35], v[48:49]
	v_accvgpr_read_b32 v25, a93
	v_max3_f32 v11, |v10|, |v25|, |v25|
	v_accvgpr_read_b32 v27, a30
	v_accvgpr_read_b32 v28, a46
	v_max3_f32 v10, |v34|, |v27|, |v28|
	v_accvgpr_read_b32 v29, a62
	v_accvgpr_read_b32 v30, a78
	v_max3_f32 v10, |v10|, |v29|, |v30|
	v_mov_b32_e32 v3, v32
	v_accvgpr_read_b32 v31, a126
	v_accvgpr_read_b32 v32, a142
	v_max3_f32 v10, |v10|, |v31|, |v32|
	v_mov_b32_e32 v18, v33
	v_mov_b32_e32 v26, v34
	v_accvgpr_read_b32 v33, a94
	v_max3_f32 v12, |v10|, |v33|, |v33|
	v_mov_b32_e32 v34, v35
	v_accvgpr_read_b32 v35, a31
	v_accvgpr_read_b32 v36, a47
	v_max3_f32 v10, |v34|, |v35|, |v36|
	v_accvgpr_read_b32 v37, a63
	v_accvgpr_read_b32 v38, a79
	v_max3_f32 v10, |v10|, |v37|, |v38|
	v_accvgpr_read_b32 v39, a127
	v_accvgpr_read_b32 v40, a143
	v_max3_f32 v10, |v10|, |v39|, |v40|
	v_accvgpr_read_b32 v41, a95
	v_max3_f32 v13, |v10|, |v41|, |v41|
	s_mov_b64 s[6:7], 0x3000
	s_nop 1
	v_max_f32_dpp v8, v8, v8 quad_perm:[1,0,3,2] row_mask:0xf bank_mask:0xf
	v_max_f32_dpp v11, v11, v11 quad_perm:[1,0,3,2] row_mask:0xf bank_mask:0xf
	v_max_f32_dpp v12, v12, v12 quad_perm:[1,0,3,2] row_mask:0xf bank_mask:0xf
	v_max_f32_dpp v13, v13, v13 quad_perm:[1,0,3,2] row_mask:0xf bank_mask:0xf
	v_max_f32_dpp v8, v8, v8 quad_perm:[2,3,0,1] row_mask:0xf bank_mask:0xf
	v_max_f32_dpp v11, v11, v11 quad_perm:[2,3,0,1] row_mask:0xf bank_mask:0xf
	v_max_f32_dpp v12, v12, v12 quad_perm:[2,3,0,1] row_mask:0xf bank_mask:0xf
	v_max_f32_dpp v13, v13, v13 quad_perm:[2,3,0,1] row_mask:0xf bank_mask:0xf
	v_max_f32_dpp v8, v8, v8 row_half_mirror row_mask:0xf bank_mask:0xf
	v_max_f32_dpp v11, v11, v11 row_half_mirror row_mask:0xf bank_mask:0xf
	v_max_f32_dpp v12, v12, v12 row_half_mirror row_mask:0xf bank_mask:0xf
	v_max_f32_dpp v13, v13, v13 row_half_mirror row_mask:0xf bank_mask:0xf
	v_max_f32_dpp v8, v8, v8 row_mirror row_mask:0xf bank_mask:0xf
	v_max_f32_dpp v11, v11, v11 row_mirror row_mask:0xf bank_mask:0xf
	v_max_f32_dpp v12, v12, v12 row_mirror row_mask:0xf bank_mask:0xf
	v_max_f32_dpp v13, v13, v13 row_mirror row_mask:0xf bank_mask:0xf
	s_nop 0
	ds_swizzle_b32 v232, v8 offset:swizzle(SWAP,16)
	ds_swizzle_b32 v233, v11 offset:swizzle(SWAP,16)
	ds_swizzle_b32 v234, v12 offset:swizzle(SWAP,16)
	ds_swizzle_b32 v235, v13 offset:swizzle(SWAP,16)
	s_waitcnt lgkmcnt(0)
	v_max_f32_e32 v10, v8, v232
	v_rcp_f32_e32 v8, v10
	v_cmp_lt_f32_e32 vcc, 0, v10
	s_waitcnt lgkmcnt(0)
	v_max_f32_e32 v11, v11, v233
	s_waitcnt lgkmcnt(0)
	v_max_f32_e32 v12, v12, v234
	v_cndmask_b32_e32 v42, 0, v8, vcc
	v_mul_f32_e32 v3, v42, v3
	v_mul_f32_e32 v6, v42, v6
	v_cvt_pknorm_i16_f32 v6, v3, v6
	v_mul_f32_e32 v3, v42, v7
	v_mul_f32_e32 v7, v42, v9
	v_cvt_pknorm_i16_f32 v7, v3, v7
	v_pk_mul_f32 v[224:225], v[14:15], v[42:43] op_sel_hi:[1,0]
	v_pk_mul_f32 v[226:227], v[16:17], v[42:43] op_sel_hi:[1,0]
	v_cvt_pknorm_i16_f32 v8, v224, v225
	v_cvt_pknorm_i16_f32 v9, v226, v227
	v_rcp_f32_e32 v3, v11
	v_cmp_lt_f32_e32 vcc, 0, v11
	v_lshl_add_u64 v[14:15], v[4:5], 0, s[6:7]
	global_store_dwordx4 v[14:15], v[6:9], off sc0 sc1
	s_mov_b64 s[6:7], 0x3200
	v_cndmask_b32_e32 v3, 0, v3, vcc
	v_pk_mul_f32 v[228:229], v[18:19], v[2:3] op_sel:[0,1] op_sel_hi:[1,1]
	v_pk_mul_f32 v[230:231], v[20:21], v[2:3] op_sel:[0,1] op_sel_hi:[1,1]
	v_cvt_pknorm_i16_f32 v6, v228, v229
	v_cvt_pknorm_i16_f32 v7, v230, v231
	v_pk_mul_f32 v[224:225], v[22:23], v[2:3] op_sel:[0,1] op_sel_hi:[1,1]
	v_pk_mul_f32 v[226:227], v[24:25], v[2:3] op_sel:[0,1] op_sel_hi:[1,1]
	v_cvt_pknorm_i16_f32 v8, v224, v225
	v_cvt_pknorm_i16_f32 v9, v226, v227
	v_rcp_f32_e32 v3, v12
	v_cmp_lt_f32_e32 vcc, 0, v12
	v_lshl_add_u64 v[14:15], v[4:5], 0, s[6:7]
	global_store_dwordx4 v[14:15], v[6:9], off sc0 sc1
	s_nop 1
	v_pk_mul_f32 v[6:7], v[10:11], s[4:5] op_sel_hi:[1,0]
	v_cndmask_b32_e32 v3, 0, v3, vcc
	global_store_dwordx2 v0, v[6:7], s[2:3] offset:96
	v_pk_mul_f32 v[228:229], v[26:27], v[2:3] op_sel:[0,1] op_sel_hi:[1,1]
	v_pk_mul_f32 v[230:231], v[28:29], v[2:3] op_sel:[0,1] op_sel_hi:[1,1]
	v_cvt_pknorm_i16_f32 v6, v228, v229
	v_cvt_pknorm_i16_f32 v7, v230, v231
	v_pk_mul_f32 v[224:225], v[30:31], v[2:3] op_sel:[0,1] op_sel_hi:[1,1]
	v_pk_mul_f32 v[226:227], v[32:33], v[2:3] op_sel:[0,1] op_sel_hi:[1,1]
	v_cvt_pknorm_i16_f32 v8, v224, v225
	s_waitcnt lgkmcnt(0)
	v_max_f32_e32 v13, v13, v235
	v_cvt_pknorm_i16_f32 v9, v226, v227
	v_rcp_f32_e32 v3, v13
	v_cmp_lt_f32_e32 vcc, 0, v13
	s_mov_b64 s[6:7], 0x3400
	v_lshl_add_u64 v[10:11], v[4:5], 0, s[6:7]
	v_cndmask_b32_e32 v3, 0, v3, vcc
	global_store_dwordx4 v[10:11], v[6:9], off sc0 sc1
	v_pk_mul_f32 v[228:229], v[34:35], v[2:3] op_sel:[0,1] op_sel_hi:[1,1]
	v_pk_mul_f32 v[230:231], v[36:37], v[2:3] op_sel:[0,1] op_sel_hi:[1,1]
	v_cvt_pknorm_i16_f32 v6, v228, v229
	v_cvt_pknorm_i16_f32 v7, v230, v231
	v_pk_mul_f32 v[224:225], v[38:39], v[2:3] op_sel:[0,1] op_sel_hi:[1,1]
	v_pk_mul_f32 v[226:227], v[40:41], v[2:3] op_sel:[0,1] op_sel_hi:[1,1]
	v_cvt_pknorm_i16_f32 v8, v224, v225
	s_mov_b64 s[6:7], 0x3600
	v_cvt_pknorm_i16_f32 v9, v226, v227
	v_lshl_add_u64 v[10:11], v[4:5], 0, s[6:7]
	global_store_dwordx4 v[10:11], v[6:9], off sc0 sc1
	s_nop 1
	v_pk_mul_f32 v[6:7], v[12:13], s[4:5] op_sel_hi:[1,0]
	global_store_dwordx2 v0, v[6:7], s[2:3] offset:104
	v_accvgpr_read_b32 v3, a240
	v_accvgpr_read_b32 v6, a224
	v_accvgpr_read_b32 v7, a208
	v_max3_f32 v8, |v3|, |v6|, |v7|
	v_accvgpr_read_b32 v9, a192
	v_accvgpr_read_b32 v14, a176
	v_max3_f32 v8, |v8|, |v9|, |v14|
	v_accvgpr_read_b32 v15, a160
	v_accvgpr_read_b32 v16, a144
	v_max3_f32 v8, |v8|, |v15|, |v16|
	v_accvgpr_read_b32 v10, a96
	v_accvgpr_read_b32 v17, a96
	v_max3_f32 v8, |v8|, |v17|, |v10|
	v_accvgpr_read_b32 v18, a241
	v_accvgpr_read_b32 v19, a225
	v_accvgpr_read_b32 v20, a209
	v_max3_f32 v10, |v18|, |v19|, |v20|
	v_accvgpr_read_b32 v21, a193
	v_accvgpr_read_b32 v22, a177
	v_max3_f32 v10, |v10|, |v21|, |v22|
	v_accvgpr_read_b32 v23, a161
	v_accvgpr_read_b32 v24, a145
	v_max3_f32 v10, |v10|, |v23|, |v24|
	v_accvgpr_read_b32 v25, a97
	v_max3_f32 v11, |v10|, |v25|, |v25|
	v_accvgpr_read_b32 v26, a242
	v_accvgpr_read_b32 v27, a226
	v_accvgpr_read_b32 v28, a210
	v_max3_f32 v10, |v26|, |v27|, |v28|
	v_accvgpr_read_b32 v29, a194
	v_accvgpr_read_b32 v30, a178
	v_max3_f32 v10, |v10|, |v29|, |v30|
	v_accvgpr_read_b32 v31, a162
	v_accvgpr_read_b32 v32, a146
	v_max3_f32 v10, |v10|, |v31|, |v32|
	v_accvgpr_read_b32 v33, a98
	v_max3_f32 v12, |v10|, |v33|, |v33|
	v_accvgpr_read_b32 v34, a243
	v_accvgpr_read_b32 v35, a227
	v_accvgpr_read_b32 v36, a211
	v_max3_f32 v10, |v34|, |v35|, |v36|
	v_accvgpr_read_b32 v37, a195
	v_accvgpr_read_b32 v38, a179
	v_max3_f32 v10, |v10|, |v37|, |v38|
	v_accvgpr_read_b32 v39, a163
	v_accvgpr_read_b32 v40, a147
	v_max3_f32 v10, |v10|, |v39|, |v40|
	v_accvgpr_read_b32 v41, a99
	v_max3_f32 v13, |v10|, |v41|, |v41|
	s_mov_b64 s[6:7], 0x4000
	s_nop 1
	v_max_f32_dpp v8, v8, v8 quad_perm:[1,0,3,2] row_mask:0xf bank_mask:0xf
	v_max_f32_dpp v11, v11, v11 quad_perm:[1,0,3,2] row_mask:0xf bank_mask:0xf
	v_max_f32_dpp v12, v12, v12 quad_perm:[1,0,3,2] row_mask:0xf bank_mask:0xf
	v_max_f32_dpp v13, v13, v13 quad_perm:[1,0,3,2] row_mask:0xf bank_mask:0xf
	v_max_f32_dpp v8, v8, v8 quad_perm:[2,3,0,1] row_mask:0xf bank_mask:0xf
	v_max_f32_dpp v11, v11, v11 quad_perm:[2,3,0,1] row_mask:0xf bank_mask:0xf
	v_max_f32_dpp v12, v12, v12 quad_perm:[2,3,0,1] row_mask:0xf bank_mask:0xf
	v_max_f32_dpp v13, v13, v13 quad_perm:[2,3,0,1] row_mask:0xf bank_mask:0xf
	v_max_f32_dpp v8, v8, v8 row_half_mirror row_mask:0xf bank_mask:0xf
	v_max_f32_dpp v11, v11, v11 row_half_mirror row_mask:0xf bank_mask:0xf
	v_max_f32_dpp v12, v12, v12 row_half_mirror row_mask:0xf bank_mask:0xf
	v_max_f32_dpp v13, v13, v13 row_half_mirror row_mask:0xf bank_mask:0xf
	v_max_f32_dpp v8, v8, v8 row_mirror row_mask:0xf bank_mask:0xf
	v_max_f32_dpp v11, v11, v11 row_mirror row_mask:0xf bank_mask:0xf
	v_max_f32_dpp v12, v12, v12 row_mirror row_mask:0xf bank_mask:0xf
	v_max_f32_dpp v13, v13, v13 row_mirror row_mask:0xf bank_mask:0xf
	s_nop 0
	ds_swizzle_b32 v232, v8 offset:swizzle(SWAP,16)
	ds_swizzle_b32 v233, v11 offset:swizzle(SWAP,16)
	ds_swizzle_b32 v234, v12 offset:swizzle(SWAP,16)
	ds_swizzle_b32 v235, v13 offset:swizzle(SWAP,16)
	s_waitcnt lgkmcnt(0)
	v_max_f32_e32 v10, v8, v232
	v_rcp_f32_e32 v8, v10
	v_cmp_lt_f32_e32 vcc, 0, v10
	s_waitcnt lgkmcnt(0)
	v_max_f32_e32 v11, v11, v233
	s_waitcnt lgkmcnt(0)
	v_max_f32_e32 v12, v12, v234
	v_cndmask_b32_e32 v42, 0, v8, vcc
	v_mul_f32_e32 v3, v42, v3
	v_mul_f32_e32 v6, v42, v6
	v_cvt_pknorm_i16_f32 v6, v3, v6
	v_mul_f32_e32 v3, v42, v7
	v_mul_f32_e32 v7, v42, v9
	v_cvt_pknorm_i16_f32 v7, v3, v7
	v_pk_mul_f32 v[228:229], v[14:15], v[42:43] op_sel_hi:[1,0]
	v_pk_mul_f32 v[230:231], v[16:17], v[42:43] op_sel_hi:[1,0]
	v_cvt_pknorm_i16_f32 v8, v228, v229
	v_cvt_pknorm_i16_f32 v9, v230, v231
	v_rcp_f32_e32 v3, v11
	v_cmp_lt_f32_e32 vcc, 0, v11
	v_lshl_add_u64 v[14:15], v[4:5], 0, s[6:7]
	global_store_dwordx4 v[14:15], v[6:9], off sc0 sc1
	s_mov_b64 s[6:7], 0x4200
	v_cndmask_b32_e32 v3, 0, v3, vcc
	v_pk_mul_f32 v[224:225], v[18:19], v[2:3] op_sel:[0,1] op_sel_hi:[1,1]
	v_pk_mul_f32 v[226:227], v[20:21], v[2:3] op_sel:[0,1] op_sel_hi:[1,1]
	v_cvt_pknorm_i16_f32 v6, v224, v225
	v_cvt_pknorm_i16_f32 v7, v226, v227
	v_pk_mul_f32 v[228:229], v[22:23], v[2:3] op_sel:[0,1] op_sel_hi:[1,1]
	v_pk_mul_f32 v[230:231], v[24:25], v[2:3] op_sel:[0,1] op_sel_hi:[1,1]
	v_cvt_pknorm_i16_f32 v8, v228, v229
	v_cvt_pknorm_i16_f32 v9, v230, v231
	v_rcp_f32_e32 v3, v12
	v_cmp_lt_f32_e32 vcc, 0, v12
	v_lshl_add_u64 v[14:15], v[4:5], 0, s[6:7]
	global_store_dwordx4 v[14:15], v[6:9], off sc0 sc1
	s_nop 1
	v_pk_mul_f32 v[6:7], v[10:11], s[4:5] op_sel_hi:[1,0]
	v_cndmask_b32_e32 v3, 0, v3, vcc
	global_store_dwordx2 v0, v[6:7], s[2:3] offset:128
	v_pk_mul_f32 v[224:225], v[26:27], v[2:3] op_sel:[0,1] op_sel_hi:[1,1]
	v_pk_mul_f32 v[226:227], v[28:29], v[2:3] op_sel:[0,1] op_sel_hi:[1,1]
	v_cvt_pknorm_i16_f32 v6, v224, v225
	v_cvt_pknorm_i16_f32 v7, v226, v227
	v_pk_mul_f32 v[228:229], v[30:31], v[2:3] op_sel:[0,1] op_sel_hi:[1,1]
	v_pk_mul_f32 v[230:231], v[32:33], v[2:3] op_sel:[0,1] op_sel_hi:[1,1]
	v_cvt_pknorm_i16_f32 v8, v228, v229
	s_waitcnt lgkmcnt(0)
	v_max_f32_e32 v13, v13, v235
	v_cvt_pknorm_i16_f32 v9, v230, v231
	v_rcp_f32_e32 v3, v13
	v_cmp_lt_f32_e32 vcc, 0, v13
	s_mov_b64 s[6:7], 0x4400
	v_lshl_add_u64 v[10:11], v[4:5], 0, s[6:7]
	v_cndmask_b32_e32 v3, 0, v3, vcc
	global_store_dwordx4 v[10:11], v[6:9], off sc0 sc1
	v_pk_mul_f32 v[224:225], v[34:35], v[2:3] op_sel:[0,1] op_sel_hi:[1,1]
	v_pk_mul_f32 v[226:227], v[36:37], v[2:3] op_sel:[0,1] op_sel_hi:[1,1]
	v_cvt_pknorm_i16_f32 v6, v224, v225
	v_cvt_pknorm_i16_f32 v7, v226, v227
	v_pk_mul_f32 v[228:229], v[38:39], v[2:3] op_sel:[0,1] op_sel_hi:[1,1]
	v_pk_mul_f32 v[230:231], v[40:41], v[2:3] op_sel:[0,1] op_sel_hi:[1,1]
	v_cvt_pknorm_i16_f32 v8, v228, v229
	s_mov_b64 s[6:7], 0x4600
	v_cvt_pknorm_i16_f32 v9, v230, v231
	v_lshl_add_u64 v[10:11], v[4:5], 0, s[6:7]
	global_store_dwordx4 v[10:11], v[6:9], off sc0 sc1
	s_nop 1
	v_pk_mul_f32 v[6:7], v[12:13], s[4:5] op_sel_hi:[1,0]
	global_store_dwordx2 v0, v[6:7], s[2:3] offset:136
	v_accvgpr_read_b32 v3, a244
	v_accvgpr_read_b32 v6, a228
	v_accvgpr_read_b32 v7, a212
	v_max3_f32 v8, |v3|, |v6|, |v7|
	v_accvgpr_read_b32 v9, a196
	v_accvgpr_read_b32 v14, a180
	v_max3_f32 v8, |v8|, |v9|, |v14|
	v_accvgpr_read_b32 v15, a164
	v_accvgpr_read_b32 v16, a148
	v_max3_f32 v8, |v8|, |v15|, |v16|
	v_accvgpr_read_b32 v10, a100
	v_accvgpr_read_b32 v17, a100
	v_max3_f32 v8, |v8|, |v17|, |v10|
	v_accvgpr_read_b32 v18, a245
	v_accvgpr_read_b32 v19, a229
	v_accvgpr_read_b32 v20, a213
	v_max3_f32 v10, |v18|, |v19|, |v20|
	v_accvgpr_read_b32 v21, a197
	v_accvgpr_read_b32 v22, a181
	v_max3_f32 v10, |v10|, |v21|, |v22|
	v_accvgpr_read_b32 v23, a165
	v_accvgpr_read_b32 v24, a149
	v_max3_f32 v10, |v10|, |v23|, |v24|
	v_accvgpr_read_b32 v25, a101
	v_max3_f32 v11, |v10|, |v25|, |v25|
	v_accvgpr_read_b32 v26, a246
	v_accvgpr_read_b32 v27, a230
	v_accvgpr_read_b32 v28, a214
	v_max3_f32 v10, |v26|, |v27|, |v28|
	v_accvgpr_read_b32 v29, a198
	v_accvgpr_read_b32 v30, a182
	v_max3_f32 v10, |v10|, |v29|, |v30|
	v_accvgpr_read_b32 v31, a166
	v_accvgpr_read_b32 v32, a150
	v_max3_f32 v10, |v10|, |v31|, |v32|
	v_accvgpr_read_b32 v33, a102
	v_max3_f32 v12, |v10|, |v33|, |v33|
	v_accvgpr_read_b32 v34, a247
	v_accvgpr_read_b32 v35, a231
	v_accvgpr_read_b32 v36, a215
	v_max3_f32 v10, |v34|, |v35|, |v36|
	v_accvgpr_read_b32 v37, a199
	v_accvgpr_read_b32 v38, a183
	v_max3_f32 v10, |v10|, |v37|, |v38|
	v_accvgpr_read_b32 v39, a167
	v_accvgpr_read_b32 v40, a151
	v_max3_f32 v10, |v10|, |v39|, |v40|
	v_accvgpr_read_b32 v41, a103
	v_max3_f32 v13, |v10|, |v41|, |v41|
	s_mov_b64 s[6:7], 0x5000
	s_nop 1
	v_max_f32_dpp v8, v8, v8 quad_perm:[1,0,3,2] row_mask:0xf bank_mask:0xf
	v_max_f32_dpp v11, v11, v11 quad_perm:[1,0,3,2] row_mask:0xf bank_mask:0xf
	v_max_f32_dpp v12, v12, v12 quad_perm:[1,0,3,2] row_mask:0xf bank_mask:0xf
	v_max_f32_dpp v13, v13, v13 quad_perm:[1,0,3,2] row_mask:0xf bank_mask:0xf
	v_max_f32_dpp v8, v8, v8 quad_perm:[2,3,0,1] row_mask:0xf bank_mask:0xf
	v_max_f32_dpp v11, v11, v11 quad_perm:[2,3,0,1] row_mask:0xf bank_mask:0xf
	v_max_f32_dpp v12, v12, v12 quad_perm:[2,3,0,1] row_mask:0xf bank_mask:0xf
	v_max_f32_dpp v13, v13, v13 quad_perm:[2,3,0,1] row_mask:0xf bank_mask:0xf
	v_max_f32_dpp v8, v8, v8 row_half_mirror row_mask:0xf bank_mask:0xf
	v_max_f32_dpp v11, v11, v11 row_half_mirror row_mask:0xf bank_mask:0xf
	v_max_f32_dpp v12, v12, v12 row_half_mirror row_mask:0xf bank_mask:0xf
	v_max_f32_dpp v13, v13, v13 row_half_mirror row_mask:0xf bank_mask:0xf
	v_max_f32_dpp v8, v8, v8 row_mirror row_mask:0xf bank_mask:0xf
	v_max_f32_dpp v11, v11, v11 row_mirror row_mask:0xf bank_mask:0xf
	v_max_f32_dpp v12, v12, v12 row_mirror row_mask:0xf bank_mask:0xf
	v_max_f32_dpp v13, v13, v13 row_mirror row_mask:0xf bank_mask:0xf
	s_nop 0
	ds_swizzle_b32 v232, v8 offset:swizzle(SWAP,16)
	ds_swizzle_b32 v233, v11 offset:swizzle(SWAP,16)
	ds_swizzle_b32 v234, v12 offset:swizzle(SWAP,16)
	ds_swizzle_b32 v235, v13 offset:swizzle(SWAP,16)
	s_waitcnt lgkmcnt(0)
	v_max_f32_e32 v10, v8, v232
	v_rcp_f32_e32 v8, v10
	v_cmp_lt_f32_e32 vcc, 0, v10
	s_waitcnt lgkmcnt(0)
	v_max_f32_e32 v11, v11, v233
	s_waitcnt lgkmcnt(0)
	v_max_f32_e32 v12, v12, v234
	v_cndmask_b32_e32 v42, 0, v8, vcc
	v_mul_f32_e32 v3, v42, v3
	v_mul_f32_e32 v6, v42, v6
	v_cvt_pknorm_i16_f32 v6, v3, v6
	v_mul_f32_e32 v3, v42, v7
	v_mul_f32_e32 v7, v42, v9
	v_cvt_pknorm_i16_f32 v7, v3, v7
	v_pk_mul_f32 v[224:225], v[14:15], v[42:43] op_sel_hi:[1,0]
	v_pk_mul_f32 v[226:227], v[16:17], v[42:43] op_sel_hi:[1,0]
	v_cvt_pknorm_i16_f32 v8, v224, v225
	v_cvt_pknorm_i16_f32 v9, v226, v227
	v_rcp_f32_e32 v3, v11
	v_cmp_lt_f32_e32 vcc, 0, v11
	v_lshl_add_u64 v[14:15], v[4:5], 0, s[6:7]
	global_store_dwordx4 v[14:15], v[6:9], off sc0 sc1
	s_mov_b64 s[6:7], 0x5200
	v_cndmask_b32_e32 v3, 0, v3, vcc
	v_pk_mul_f32 v[228:229], v[18:19], v[2:3] op_sel:[0,1] op_sel_hi:[1,1]
	v_pk_mul_f32 v[230:231], v[20:21], v[2:3] op_sel:[0,1] op_sel_hi:[1,1]
	v_cvt_pknorm_i16_f32 v6, v228, v229
	v_cvt_pknorm_i16_f32 v7, v230, v231
	v_pk_mul_f32 v[224:225], v[22:23], v[2:3] op_sel:[0,1] op_sel_hi:[1,1]
	v_pk_mul_f32 v[226:227], v[24:25], v[2:3] op_sel:[0,1] op_sel_hi:[1,1]
	v_cvt_pknorm_i16_f32 v8, v224, v225
	v_cvt_pknorm_i16_f32 v9, v226, v227
	v_rcp_f32_e32 v3, v12
	v_cmp_lt_f32_e32 vcc, 0, v12
	v_lshl_add_u64 v[14:15], v[4:5], 0, s[6:7]
	global_store_dwordx4 v[14:15], v[6:9], off sc0 sc1
	s_nop 1
	v_pk_mul_f32 v[6:7], v[10:11], s[4:5] op_sel_hi:[1,0]
	v_cndmask_b32_e32 v3, 0, v3, vcc
	global_store_dwordx2 v0, v[6:7], s[2:3] offset:160
	v_pk_mul_f32 v[228:229], v[26:27], v[2:3] op_sel:[0,1] op_sel_hi:[1,1]
	v_pk_mul_f32 v[230:231], v[28:29], v[2:3] op_sel:[0,1] op_sel_hi:[1,1]
	v_cvt_pknorm_i16_f32 v6, v228, v229
	v_cvt_pknorm_i16_f32 v7, v230, v231
	v_pk_mul_f32 v[224:225], v[30:31], v[2:3] op_sel:[0,1] op_sel_hi:[1,1]
	v_pk_mul_f32 v[226:227], v[32:33], v[2:3] op_sel:[0,1] op_sel_hi:[1,1]
	v_cvt_pknorm_i16_f32 v8, v224, v225
	s_waitcnt lgkmcnt(0)
	v_max_f32_e32 v13, v13, v235
	v_cvt_pknorm_i16_f32 v9, v226, v227
	v_rcp_f32_e32 v3, v13
	v_cmp_lt_f32_e32 vcc, 0, v13
	s_mov_b64 s[6:7], 0x5400
	v_lshl_add_u64 v[10:11], v[4:5], 0, s[6:7]
	v_cndmask_b32_e32 v3, 0, v3, vcc
	global_store_dwordx4 v[10:11], v[6:9], off sc0 sc1
	v_pk_mul_f32 v[228:229], v[34:35], v[2:3] op_sel:[0,1] op_sel_hi:[1,1]
	v_pk_mul_f32 v[230:231], v[36:37], v[2:3] op_sel:[0,1] op_sel_hi:[1,1]
	v_cvt_pknorm_i16_f32 v6, v228, v229
	v_cvt_pknorm_i16_f32 v7, v230, v231
	v_pk_mul_f32 v[224:225], v[38:39], v[2:3] op_sel:[0,1] op_sel_hi:[1,1]
	v_pk_mul_f32 v[226:227], v[40:41], v[2:3] op_sel:[0,1] op_sel_hi:[1,1]
	v_cvt_pknorm_i16_f32 v8, v224, v225
	s_mov_b64 s[6:7], 0x5600
	v_cvt_pknorm_i16_f32 v9, v226, v227
	v_lshl_add_u64 v[10:11], v[4:5], 0, s[6:7]
	global_store_dwordx4 v[10:11], v[6:9], off sc0 sc1
	s_nop 1
	v_pk_mul_f32 v[6:7], v[12:13], s[4:5] op_sel_hi:[1,0]
	global_store_dwordx2 v0, v[6:7], s[2:3] offset:168
	v_accvgpr_read_b32 v3, a248
	v_accvgpr_read_b32 v6, a232
	v_accvgpr_read_b32 v7, a216
	v_max3_f32 v8, |v3|, |v6|, |v7|
	v_accvgpr_read_b32 v9, a200
	v_accvgpr_read_b32 v14, a184
	v_max3_f32 v8, |v8|, |v9|, |v14|
	v_accvgpr_read_b32 v15, a168
	v_accvgpr_read_b32 v16, a152
	v_max3_f32 v8, |v8|, |v15|, |v16|
	v_accvgpr_read_b32 v10, a104
	v_accvgpr_read_b32 v17, a104
	v_max3_f32 v8, |v8|, |v17|, |v10|
	v_accvgpr_read_b32 v18, a249
	v_accvgpr_read_b32 v19, a233
	v_accvgpr_read_b32 v20, a217
	v_max3_f32 v10, |v18|, |v19|, |v20|
	v_accvgpr_read_b32 v21, a201
	v_accvgpr_read_b32 v22, a185
	v_max3_f32 v10, |v10|, |v21|, |v22|
	v_accvgpr_read_b32 v23, a169
	v_accvgpr_read_b32 v24, a153
	v_max3_f32 v10, |v10|, |v23|, |v24|
	v_accvgpr_read_b32 v25, a105
	v_max3_f32 v11, |v10|, |v25|, |v25|
	v_accvgpr_read_b32 v26, a250
	v_accvgpr_read_b32 v27, a234
	v_accvgpr_read_b32 v28, a218
	v_max3_f32 v10, |v26|, |v27|, |v28|
	v_accvgpr_read_b32 v29, a202
	v_accvgpr_read_b32 v30, a186
	v_max3_f32 v10, |v10|, |v29|, |v30|
	v_accvgpr_read_b32 v31, a170
	v_accvgpr_read_b32 v32, a154
	v_max3_f32 v10, |v10|, |v31|, |v32|
	v_accvgpr_read_b32 v33, a106
	v_max3_f32 v12, |v10|, |v33|, |v33|
	v_accvgpr_read_b32 v34, a251
	v_accvgpr_read_b32 v35, a235
	v_accvgpr_read_b32 v36, a219
	v_max3_f32 v10, |v34|, |v35|, |v36|
	v_accvgpr_read_b32 v37, a203
	v_accvgpr_read_b32 v38, a187
	v_max3_f32 v10, |v10|, |v37|, |v38|
	v_accvgpr_read_b32 v39, a171
	v_accvgpr_read_b32 v40, a155
	v_max3_f32 v10, |v10|, |v39|, |v40|
	v_accvgpr_read_b32 v41, a107
	v_max3_f32 v13, |v10|, |v41|, |v41|
	s_mov_b64 s[6:7], 0x6000
	s_nop 1
	v_max_f32_dpp v8, v8, v8 quad_perm:[1,0,3,2] row_mask:0xf bank_mask:0xf
	v_max_f32_dpp v11, v11, v11 quad_perm:[1,0,3,2] row_mask:0xf bank_mask:0xf
	v_max_f32_dpp v12, v12, v12 quad_perm:[1,0,3,2] row_mask:0xf bank_mask:0xf
	v_max_f32_dpp v13, v13, v13 quad_perm:[1,0,3,2] row_mask:0xf bank_mask:0xf
	v_max_f32_dpp v8, v8, v8 quad_perm:[2,3,0,1] row_mask:0xf bank_mask:0xf
	v_max_f32_dpp v11, v11, v11 quad_perm:[2,3,0,1] row_mask:0xf bank_mask:0xf
	v_max_f32_dpp v12, v12, v12 quad_perm:[2,3,0,1] row_mask:0xf bank_mask:0xf
	v_max_f32_dpp v13, v13, v13 quad_perm:[2,3,0,1] row_mask:0xf bank_mask:0xf
	v_max_f32_dpp v8, v8, v8 row_half_mirror row_mask:0xf bank_mask:0xf
	v_max_f32_dpp v11, v11, v11 row_half_mirror row_mask:0xf bank_mask:0xf
	v_max_f32_dpp v12, v12, v12 row_half_mirror row_mask:0xf bank_mask:0xf
	v_max_f32_dpp v13, v13, v13 row_half_mirror row_mask:0xf bank_mask:0xf
	v_max_f32_dpp v8, v8, v8 row_mirror row_mask:0xf bank_mask:0xf
	v_max_f32_dpp v11, v11, v11 row_mirror row_mask:0xf bank_mask:0xf
	v_max_f32_dpp v12, v12, v12 row_mirror row_mask:0xf bank_mask:0xf
	v_max_f32_dpp v13, v13, v13 row_mirror row_mask:0xf bank_mask:0xf
	s_nop 0
	ds_swizzle_b32 v232, v8 offset:swizzle(SWAP,16)
	ds_swizzle_b32 v233, v11 offset:swizzle(SWAP,16)
	ds_swizzle_b32 v234, v12 offset:swizzle(SWAP,16)
	ds_swizzle_b32 v235, v13 offset:swizzle(SWAP,16)
	s_waitcnt lgkmcnt(0)
	v_max_f32_e32 v10, v8, v232
	v_rcp_f32_e32 v8, v10
	v_cmp_lt_f32_e32 vcc, 0, v10
	s_waitcnt lgkmcnt(0)
	v_max_f32_e32 v11, v11, v233
	s_waitcnt lgkmcnt(0)
	v_max_f32_e32 v12, v12, v234
	v_cndmask_b32_e32 v42, 0, v8, vcc
	v_mul_f32_e32 v3, v42, v3
	v_mul_f32_e32 v6, v42, v6
	v_cvt_pknorm_i16_f32 v6, v3, v6
	v_mul_f32_e32 v3, v42, v7
	v_mul_f32_e32 v7, v42, v9
	v_cvt_pknorm_i16_f32 v7, v3, v7
	v_pk_mul_f32 v[228:229], v[14:15], v[42:43] op_sel_hi:[1,0]
	v_pk_mul_f32 v[230:231], v[16:17], v[42:43] op_sel_hi:[1,0]
	v_cvt_pknorm_i16_f32 v8, v228, v229
	v_cvt_pknorm_i16_f32 v9, v230, v231
	v_rcp_f32_e32 v3, v11
	v_cmp_lt_f32_e32 vcc, 0, v11
	v_lshl_add_u64 v[14:15], v[4:5], 0, s[6:7]
	global_store_dwordx4 v[14:15], v[6:9], off sc0 sc1
	s_mov_b64 s[6:7], 0x6200
	v_cndmask_b32_e32 v3, 0, v3, vcc
	v_pk_mul_f32 v[224:225], v[18:19], v[2:3] op_sel:[0,1] op_sel_hi:[1,1]
	v_pk_mul_f32 v[226:227], v[20:21], v[2:3] op_sel:[0,1] op_sel_hi:[1,1]
	v_cvt_pknorm_i16_f32 v6, v224, v225
	v_cvt_pknorm_i16_f32 v7, v226, v227
	v_pk_mul_f32 v[228:229], v[22:23], v[2:3] op_sel:[0,1] op_sel_hi:[1,1]
	v_pk_mul_f32 v[230:231], v[24:25], v[2:3] op_sel:[0,1] op_sel_hi:[1,1]
	v_cvt_pknorm_i16_f32 v8, v228, v229
	v_cvt_pknorm_i16_f32 v9, v230, v231
	v_rcp_f32_e32 v3, v12
	v_cmp_lt_f32_e32 vcc, 0, v12
	v_lshl_add_u64 v[14:15], v[4:5], 0, s[6:7]
	global_store_dwordx4 v[14:15], v[6:9], off sc0 sc1
	s_nop 1
	v_pk_mul_f32 v[6:7], v[10:11], s[4:5] op_sel_hi:[1,0]
	v_cndmask_b32_e32 v3, 0, v3, vcc
	global_store_dwordx2 v0, v[6:7], s[2:3] offset:192
	v_pk_mul_f32 v[224:225], v[26:27], v[2:3] op_sel:[0,1] op_sel_hi:[1,1]
	v_pk_mul_f32 v[226:227], v[28:29], v[2:3] op_sel:[0,1] op_sel_hi:[1,1]
	v_cvt_pknorm_i16_f32 v6, v224, v225
	v_cvt_pknorm_i16_f32 v7, v226, v227
	v_pk_mul_f32 v[228:229], v[30:31], v[2:3] op_sel:[0,1] op_sel_hi:[1,1]
	v_pk_mul_f32 v[230:231], v[32:33], v[2:3] op_sel:[0,1] op_sel_hi:[1,1]
	v_cvt_pknorm_i16_f32 v8, v228, v229
	s_waitcnt lgkmcnt(0)
	v_max_f32_e32 v13, v13, v235
	v_cvt_pknorm_i16_f32 v9, v230, v231
	v_rcp_f32_e32 v3, v13
	v_cmp_lt_f32_e32 vcc, 0, v13
	s_mov_b64 s[6:7], 0x6400
	v_lshl_add_u64 v[10:11], v[4:5], 0, s[6:7]
	v_cndmask_b32_e32 v3, 0, v3, vcc
	global_store_dwordx4 v[10:11], v[6:9], off sc0 sc1
	v_pk_mul_f32 v[224:225], v[34:35], v[2:3] op_sel:[0,1] op_sel_hi:[1,1]
	v_pk_mul_f32 v[226:227], v[36:37], v[2:3] op_sel:[0,1] op_sel_hi:[1,1]
	v_cvt_pknorm_i16_f32 v6, v224, v225
	v_cvt_pknorm_i16_f32 v7, v226, v227
	v_pk_mul_f32 v[228:229], v[38:39], v[2:3] op_sel:[0,1] op_sel_hi:[1,1]
	v_pk_mul_f32 v[230:231], v[40:41], v[2:3] op_sel:[0,1] op_sel_hi:[1,1]
	v_cvt_pknorm_i16_f32 v8, v228, v229
	s_mov_b64 s[6:7], 0x6600
	v_cvt_pknorm_i16_f32 v9, v230, v231
	v_lshl_add_u64 v[10:11], v[4:5], 0, s[6:7]
	global_store_dwordx4 v[10:11], v[6:9], off sc0 sc1
	s_nop 1
	v_pk_mul_f32 v[6:7], v[12:13], s[4:5] op_sel_hi:[1,0]
	global_store_dwordx2 v0, v[6:7], s[2:3] offset:200
	v_accvgpr_read_b32 v3, a252
	v_accvgpr_read_b32 v6, a236
	v_accvgpr_read_b32 v7, a220
	v_max3_f32 v8, |v3|, |v6|, |v7|
	v_accvgpr_read_b32 v9, a204
	v_accvgpr_read_b32 v14, a188
	v_max3_f32 v8, |v8|, |v9|, |v14|
	v_accvgpr_read_b32 v15, a172
	v_accvgpr_read_b32 v16, a156
	v_max3_f32 v8, |v8|, |v15|, |v16|
	v_accvgpr_read_b32 v10, a108
	v_accvgpr_read_b32 v17, a108
	v_max3_f32 v8, |v8|, |v17|, |v10|
	v_accvgpr_read_b32 v18, a253
	v_accvgpr_read_b32 v19, a237
	v_accvgpr_read_b32 v20, a221
	v_max3_f32 v10, |v18|, |v19|, |v20|
	v_accvgpr_read_b32 v21, a205
	v_accvgpr_read_b32 v22, a189
	v_max3_f32 v10, |v10|, |v21|, |v22|
	v_accvgpr_read_b32 v23, a173
	v_accvgpr_read_b32 v24, a157
	v_max3_f32 v10, |v10|, |v23|, |v24|
	v_accvgpr_read_b32 v25, a109
	v_max3_f32 v11, |v10|, |v25|, |v25|
	v_accvgpr_read_b32 v26, a254
	v_accvgpr_read_b32 v27, a238
	v_accvgpr_read_b32 v28, a222
	v_max3_f32 v10, |v26|, |v27|, |v28|
	v_accvgpr_read_b32 v29, a206
	v_accvgpr_read_b32 v30, a190
	v_max3_f32 v10, |v10|, |v29|, |v30|
	v_accvgpr_read_b32 v31, a174
	v_accvgpr_read_b32 v32, a158
	v_max3_f32 v10, |v10|, |v31|, |v32|
	v_accvgpr_read_b32 v33, a110
	v_max3_f32 v12, |v10|, |v33|, |v33|
	v_accvgpr_read_b32 v34, a255
	v_accvgpr_read_b32 v35, a239
	v_accvgpr_read_b32 v36, a223
	v_max3_f32 v10, |v34|, |v35|, |v36|
	v_accvgpr_read_b32 v37, a207
	v_accvgpr_read_b32 v38, a191
	v_max3_f32 v10, |v10|, |v37|, |v38|
	v_accvgpr_read_b32 v39, a175
	v_accvgpr_read_b32 v40, a159
	v_max3_f32 v10, |v10|, |v39|, |v40|
	v_accvgpr_read_b32 v41, a111
	v_max3_f32 v13, |v10|, |v41|, |v41|
	s_mov_b64 s[6:7], 0x7000
	s_nop 1
	v_max_f32_dpp v8, v8, v8 quad_perm:[1,0,3,2] row_mask:0xf bank_mask:0xf
	v_max_f32_dpp v11, v11, v11 quad_perm:[1,0,3,2] row_mask:0xf bank_mask:0xf
	v_max_f32_dpp v12, v12, v12 quad_perm:[1,0,3,2] row_mask:0xf bank_mask:0xf
	v_max_f32_dpp v13, v13, v13 quad_perm:[1,0,3,2] row_mask:0xf bank_mask:0xf
	v_max_f32_dpp v8, v8, v8 quad_perm:[2,3,0,1] row_mask:0xf bank_mask:0xf
	v_max_f32_dpp v11, v11, v11 quad_perm:[2,3,0,1] row_mask:0xf bank_mask:0xf
	v_max_f32_dpp v12, v12, v12 quad_perm:[2,3,0,1] row_mask:0xf bank_mask:0xf
	v_max_f32_dpp v13, v13, v13 quad_perm:[2,3,0,1] row_mask:0xf bank_mask:0xf
	v_max_f32_dpp v8, v8, v8 row_half_mirror row_mask:0xf bank_mask:0xf
	v_max_f32_dpp v11, v11, v11 row_half_mirror row_mask:0xf bank_mask:0xf
	v_max_f32_dpp v12, v12, v12 row_half_mirror row_mask:0xf bank_mask:0xf
	v_max_f32_dpp v13, v13, v13 row_half_mirror row_mask:0xf bank_mask:0xf
	v_max_f32_dpp v8, v8, v8 row_mirror row_mask:0xf bank_mask:0xf
	v_max_f32_dpp v11, v11, v11 row_mirror row_mask:0xf bank_mask:0xf
	v_max_f32_dpp v12, v12, v12 row_mirror row_mask:0xf bank_mask:0xf
	v_max_f32_dpp v13, v13, v13 row_mirror row_mask:0xf bank_mask:0xf
	s_nop 0
	ds_swizzle_b32 v232, v8 offset:swizzle(SWAP,16)
	ds_swizzle_b32 v233, v11 offset:swizzle(SWAP,16)
	ds_swizzle_b32 v234, v12 offset:swizzle(SWAP,16)
	ds_swizzle_b32 v235, v13 offset:swizzle(SWAP,16)
	s_waitcnt lgkmcnt(0)
	v_max_f32_e32 v10, v8, v232
	v_rcp_f32_e32 v8, v10
	v_cmp_lt_f32_e32 vcc, 0, v10
	s_waitcnt lgkmcnt(0)
	v_max_f32_e32 v11, v11, v233
	s_waitcnt lgkmcnt(0)
	v_max_f32_e32 v12, v12, v234
	v_cndmask_b32_e32 v42, 0, v8, vcc
	v_mul_f32_e32 v3, v42, v3
	v_mul_f32_e32 v6, v42, v6
	v_cvt_pknorm_i16_f32 v6, v3, v6
	v_mul_f32_e32 v3, v42, v7
	v_mul_f32_e32 v7, v42, v9
	v_cvt_pknorm_i16_f32 v7, v3, v7
	v_pk_mul_f32 v[224:225], v[14:15], v[42:43] op_sel_hi:[1,0]
	v_pk_mul_f32 v[226:227], v[16:17], v[42:43] op_sel_hi:[1,0]
	v_cvt_pknorm_i16_f32 v8, v224, v225
	v_cvt_pknorm_i16_f32 v9, v226, v227
	v_rcp_f32_e32 v3, v11
	v_cmp_lt_f32_e32 vcc, 0, v11
	v_lshl_add_u64 v[14:15], v[4:5], 0, s[6:7]
	global_store_dwordx4 v[14:15], v[6:9], off sc0 sc1
	s_mov_b64 s[6:7], 0x7200
	v_cndmask_b32_e32 v3, 0, v3, vcc
	v_pk_mul_f32 v[228:229], v[18:19], v[2:3] op_sel:[0,1] op_sel_hi:[1,1]
	v_pk_mul_f32 v[230:231], v[20:21], v[2:3] op_sel:[0,1] op_sel_hi:[1,1]
	v_cvt_pknorm_i16_f32 v6, v228, v229
	v_cvt_pknorm_i16_f32 v7, v230, v231
	v_pk_mul_f32 v[224:225], v[22:23], v[2:3] op_sel:[0,1] op_sel_hi:[1,1]
	v_pk_mul_f32 v[226:227], v[24:25], v[2:3] op_sel:[0,1] op_sel_hi:[1,1]
	v_cvt_pknorm_i16_f32 v8, v224, v225
	v_cvt_pknorm_i16_f32 v9, v226, v227
	v_rcp_f32_e32 v3, v12
	v_cmp_lt_f32_e32 vcc, 0, v12
	v_lshl_add_u64 v[14:15], v[4:5], 0, s[6:7]
	global_store_dwordx4 v[14:15], v[6:9], off sc0 sc1
	s_nop 1
	v_pk_mul_f32 v[6:7], v[10:11], s[4:5] op_sel_hi:[1,0]
	v_cndmask_b32_e32 v3, 0, v3, vcc
	global_store_dwordx2 v0, v[6:7], s[2:3] offset:224
	v_pk_mul_f32 v[228:229], v[26:27], v[2:3] op_sel:[0,1] op_sel_hi:[1,1]
	v_pk_mul_f32 v[230:231], v[28:29], v[2:3] op_sel:[0,1] op_sel_hi:[1,1]
	v_cvt_pknorm_i16_f32 v6, v228, v229
	v_cvt_pknorm_i16_f32 v7, v230, v231
	v_pk_mul_f32 v[224:225], v[30:31], v[2:3] op_sel:[0,1] op_sel_hi:[1,1]
	v_pk_mul_f32 v[226:227], v[32:33], v[2:3] op_sel:[0,1] op_sel_hi:[1,1]
	v_cvt_pknorm_i16_f32 v8, v224, v225
	s_waitcnt lgkmcnt(0)
	v_max_f32_e32 v13, v13, v235
	v_cvt_pknorm_i16_f32 v9, v226, v227
	v_rcp_f32_e32 v3, v13
	v_cmp_lt_f32_e32 vcc, 0, v13
	s_mov_b64 s[6:7], 0x7400
	v_lshl_add_u64 v[10:11], v[4:5], 0, s[6:7]
	v_cndmask_b32_e32 v3, 0, v3, vcc
	global_store_dwordx4 v[10:11], v[6:9], off sc0 sc1
	v_pk_mul_f32 v[228:229], v[34:35], v[2:3] op_sel:[0,1] op_sel_hi:[1,1]
	v_pk_mul_f32 v[230:231], v[36:37], v[2:3] op_sel:[0,1] op_sel_hi:[1,1]
	v_cvt_pknorm_i16_f32 v6, v228, v229
	v_cvt_pknorm_i16_f32 v7, v230, v231
	v_pk_mul_f32 v[224:225], v[38:39], v[2:3] op_sel:[0,1] op_sel_hi:[1,1]
	v_pk_mul_f32 v[226:227], v[40:41], v[2:3] op_sel:[0,1] op_sel_hi:[1,1]
	v_cvt_pknorm_i16_f32 v8, v224, v225
	s_mov_b64 s[6:7], 0x7600
	v_cvt_pknorm_i16_f32 v9, v226, v227
	v_lshl_add_u64 v[4:5], v[4:5], 0, s[6:7]
	global_store_dwordx4 v[4:5], v[6:9], off sc0 sc1
	v_pk_mul_f32 v[4:5], v[12:13], s[4:5] op_sel_hi:[1,0]
	global_store_dwordx2 v0, v[4:5], s[2:3] offset:232
	ds_bpermute_b32 v4, v133, v134
	s_lshl_b64 s[0:1], s[0:1], 2
	s_add_u32 s0, s26, s0
	s_addc_u32 s1, s27, s1
	v_mov_b32_e32 v3, v1
	v_cmp_gt_i32_e32 vcc, 32, v132
	v_lshl_add_u64 v[0:1], s[0:1], 0, v[2:3]
	s_and_saveexec_b64 s[0:1], vcc
	s_cbranch_execz .LBB1_6
	s_waitcnt lgkmcnt(0)
	v_add_f32_e32 v2, v134, v4
	global_store_dword v[0:1], v2, off
